# m5 with XP5 160 (more w_down items beside the scan now that converters start before the barrier completes)
# baseline (speedup 1.0000x reference)
; #define LAS __attribute__((address_space(3)))
; __device__ __forceinline__ void cvt_item_lds(const float* src, int ld_src, fp8_t* dst, int ld_dst, LAS unsigned char* lds, int tid, int wv) {
;     const int lane = tid & 63;
;     const float* s = src + (size_t)(16 * wv) * ld_src + 4 * lane;
;     f32x4 va[16], vb[16];
;     cvt8_load(va, s, ld_src);
; #pragma unroll
;     for (int t = 0; t < 8; t += 2) {
;         cvt8_load(vb, s + (t + 1) * 256, ld_src); __builtin_amdgcn_sched_barrier(0);
; __device__ __forceinline__ void conv_queue(const Params& p, LAS unsigned char* lds, const int wave, const int cw, const int first, const int last, const int slot_off = LDS_MISC) {
;     ...
;     for (;;) {
;         __syncthreads();
;         if (tid == 0) *slot = first + (int)atomicAdd(&p.ctl[cw], 1u);
;         __syncthreads();
;         const int it = *slot;
;         if (it >= last) break;
;         if (it < N_GU) { const int e = it >> 5, rem = it & 31, kb = rem >> 1, nh = rem & 1;
;             const float* src = p.w_gu + (size_t)e * ND * (2 * DFF) + (size_t)(kb * 128) * (2 * DFF) + nh * 2048;
;             fp8_t* dst = p.wt_gu + (size_t)e * (2 * DFF) * ND + (size_t)(nh * 2048) * ND + kb * 128;
;             cvt_item_lds(src, 2 * DFF, dst, ND, lds, tid, wave); }
;         else { const int j = it - N_GU, e = j >> 4, kb = j & 15;
;             const float* src = p.w_down + (size_t)e * DFF * ND + (size_t)(kb * 128) * ND;
;             fp8_t* dst = p.wt_down + (size_t)e * ND * DFF + kb * 128;
;             cvt_item_lds(src, ND, dst, DFF, lds, tid, wave); }
.LBB0_822:
	s_or_b64 exec, exec, s[48:49]
	s_waitcnt lgkmcnt(0)
	s_barrier
	ds_read_b32 v0, v209
	s_movk_i32 s2, 0x49f
	s_mov_b64 s[48:49], -1
	s_waitcnt lgkmcnt(0)
	v_cmp_lt_i32_e32 vcc, s2, v0
	v_readfirstlane_b32 s33, v0
	s_cbranch_vccnz .LBB0_817
	s_cmpk_gt_i32 s33, 0x3ff
	s_cbranch_scc0 .LBB0_825
	s_add_i32 s2, s33, 0xfffffc00
	s_lshr_b32 s4, s2, 4
	v_readlane_b32 s16, v254, 22
	s_lshl_b64 s[34:35], s[4:5], 22
	s_lshl_b64 s[48:49], s[4:5], 24
	v_readlane_b32 s20, v254, 26
	v_readlane_b32 s21, v254, 27
	s_add_u32 s2, s20, s48
	s_addc_u32 s4, s21, s49
	s_lshl_b32 s48, s33, 7
	s_and_b32 s48, s48, 0x780
	s_lshl_b32 s49, s48, 13
	s_add_u32 s2, s2, s49
	s_addc_u32 s4, s4, 0
	s_add_u32 s34, s56, s34
	s_addc_u32 s35, s57, s35
	s_add_u32 s50, s34, s48
	s_addc_u32 s51, s35, 0
	s_add_u32 s48, s2, s14
	s_addc_u32 s49, s4, s15
	v_lshl_add_u64 v[172:173], s[48:49], 0, v[128:129]
	s_movk_i32 s2, 0x2000
	v_add_co_u32_e32 v174, vcc, s2, v172
	s_movk_i32 s2, 0x3000
	s_nop 0
	v_addc_co_u32_e32 v175, vcc, 0, v173, vcc
	v_add_co_u32_e32 v142, vcc, s2, v172
	s_movk_i32 s2, 0x6000
	s_nop 0
	v_addc_co_u32_e32 v143, vcc, 0, v173, vcc
	v_add_co_u32_e32 v176, vcc, s13, v172
	v_readlane_b32 s17, v254, 23
	s_nop 0
	v_addc_co_u32_e32 v177, vcc, 0, v173, vcc
	v_add_co_u32_e32 v144, vcc, s67, v172
	v_readlane_b32 s18, v254, 24
	s_nop 0
	v_addc_co_u32_e32 v145, vcc, 0, v173, vcc
	v_add_co_u32_e32 v178, vcc, s2, v172
	s_movk_i32 s2, 0x7000
	s_nop 0
	v_addc_co_u32_e32 v179, vcc, 0, v173, vcc
	v_add_co_u32_e32 v146, vcc, s2, v172
	s_mov_b32 s2, 0xa000
	s_nop 0
	v_addc_co_u32_e32 v147, vcc, 0, v173, vcc
	v_add_co_u32_e32 v180, vcc, s60, v172
	global_load_dwordx4 v[16:19], v[144:145], off offset:-4096 nt
	global_load_dwordx4 v[20:23], v[146:147], off offset:-4096 nt
	v_addc_co_u32_e32 v181, vcc, 0, v173, vcc
	v_add_co_u32_e32 v148, vcc, s68, v172
	v_readlane_b32 s19, v254, 25
	s_nop 0
	v_addc_co_u32_e32 v149, vcc, 0, v173, vcc
	v_add_co_u32_e32 v182, vcc, s2, v172
	s_mov_b32 s2, 0xb000
	s_nop 0
	v_addc_co_u32_e32 v183, vcc, 0, v173, vcc
	v_add_co_u32_e32 v150, vcc, s2, v172
	s_mov_b32 s2, 0xe000
	s_nop 0
	v_addc_co_u32_e32 v151, vcc, 0, v173, vcc
	v_add_co_u32_e32 v184, vcc, s61, v172
	global_load_dwordx4 v[24:27], v[148:149], off offset:-4096 nt
	global_load_dwordx4 v[28:31], v[150:151], off offset:-4096 nt
	v_addc_co_u32_e32 v185, vcc, 0, v173, vcc
	v_add_co_u32_e32 v152, vcc, s69, v172
	v_readlane_b32 s22, v254, 28
	s_nop 0
	v_addc_co_u32_e32 v153, vcc, 0, v173, vcc
	v_add_co_u32_e32 v186, vcc, s2, v172
	s_mov_b32 s2, 0xf000
	s_nop 0
	v_addc_co_u32_e32 v187, vcc, 0, v173, vcc
	v_add_co_u32_e32 v154, vcc, s2, v172
	s_mov_b32 s2, 0x12000
	s_nop 0
	v_addc_co_u32_e32 v155, vcc, 0, v173, vcc
	v_add_co_u32_e32 v188, vcc, s62, v172
	global_load_dwordx4 v[56:59], v[152:153], off offset:-4096 nt
	global_load_dwordx4 v[60:63], v[154:155], off offset:-4096 nt
	v_addc_co_u32_e32 v189, vcc, 0, v173, vcc
	v_add_co_u32_e32 v156, vcc, s88, v172
	v_readlane_b32 s23, v254, 29
	s_nop 0
	v_addc_co_u32_e32 v157, vcc, 0, v173, vcc
	v_add_co_u32_e32 v190, vcc, s2, v172
	s_mov_b32 s2, 0x13000
	s_nop 0
	v_addc_co_u32_e32 v191, vcc, 0, v173, vcc
	v_add_co_u32_e32 v158, vcc, s2, v172
	s_mov_b32 s2, 0x16000
	s_nop 0
	v_addc_co_u32_e32 v159, vcc, 0, v173, vcc
	v_add_co_u32_e32 v192, vcc, s63, v172
	global_load_dwordx4 v[48:51], v[156:157], off offset:-4096 nt
	global_load_dwordx4 v[52:55], v[158:159], off offset:-4096 nt
	v_addc_co_u32_e32 v193, vcc, 0, v173, vcc
	v_add_co_u32_e32 v160, vcc, s89, v172
	v_readlane_b32 s24, v254, 30
	s_nop 0
	v_addc_co_u32_e32 v161, vcc, 0, v173, vcc
	v_add_co_u32_e32 v194, vcc, s2, v172
	s_mov_b32 s2, 0x17000
	s_nop 0
	v_addc_co_u32_e32 v195, vcc, 0, v173, vcc
	v_add_co_u32_e32 v162, vcc, s2, v172
	s_mov_b32 s2, 0x1a000
	s_nop 0
	v_addc_co_u32_e32 v163, vcc, 0, v173, vcc
	v_add_co_u32_e32 v196, vcc, s64, v172
	global_load_dwordx4 v[80:83], v[160:161], off offset:-4096 nt
	global_load_dwordx4 v[84:87], v[162:163], off offset:-4096 nt
	v_addc_co_u32_e32 v197, vcc, 0, v173, vcc
	v_add_co_u32_e32 v164, vcc, s90, v172
	v_readlane_b32 s25, v254, 31
	s_nop 0
	v_addc_co_u32_e32 v165, vcc, 0, v173, vcc
	v_add_co_u32_e32 v198, vcc, s2, v172
	s_mov_b32 s2, 0x1b000
	s_nop 0
	v_addc_co_u32_e32 v199, vcc, 0, v173, vcc
	v_add_co_u32_e32 v166, vcc, s2, v172
	s_mov_b32 s2, 0x1e000
	s_nop 0
	v_addc_co_u32_e32 v167, vcc, 0, v173, vcc
	v_add_co_u32_e32 v200, vcc, s65, v172
	global_load_dwordx4 v[88:91], v[164:165], off offset:-4096 nt
	global_load_dwordx4 v[92:95], v[166:167], off offset:-4096 nt
	v_addc_co_u32_e32 v201, vcc, 0, v173, vcc
	v_add_co_u32_e32 v168, vcc, s91, v172
	v_readlane_b32 s26, v254, 32
	s_nop 0
	v_addc_co_u32_e32 v169, vcc, 0, v173, vcc
	v_add_co_u32_e32 v202, vcc, s2, v172
	s_mov_b32 s2, 0x1f000
	s_nop 0
	v_addc_co_u32_e32 v203, vcc, 0, v173, vcc
	v_add_co_u32_e32 v170, vcc, s2, v172
	v_readlane_b32 s27, v254, 33
	s_nop 0
	v_addc_co_u32_e32 v171, vcc, 0, v173, vcc
	global_load_dwordx4 v[108:111], v[168:169], off offset:-4096 nt
	global_load_dwordx4 v[112:115], v[170:171], off offset:-4096 nt
	global_load_dwordx4 v[116:119], v[142:143], off offset:-4096 nt
	global_load_dwordx4 v[96:99], v128, s[48:49] offset:1024 nt
	global_load_dwordx4 v[100:103], v[174:175], off offset:1024 nt
	global_load_dwordx4 v[104:107], v[176:177], off offset:1024 nt
	global_load_dwordx4 v[124:127], v[178:179], off offset:1024 nt
	global_load_dwordx4 v[64:67], v[180:181], off offset:1024 nt
	global_load_dwordx4 v[68:71], v[182:183], off offset:1024 nt
	global_load_dwordx4 v[72:75], v[184:185], off offset:1024 nt
	global_load_dwordx4 v[76:79], v[186:187], off offset:1024 nt
	global_load_dwordx4 v[32:35], v[188:189], off offset:1024 nt
	global_load_dwordx4 v[36:39], v[190:191], off offset:1024 nt
	global_load_dwordx4 v[40:43], v[192:193], off offset:1024 nt
	global_load_dwordx4 v[44:47], v[194:195], off offset:1024 nt
	global_load_dwordx4 v[0:3], v[196:197], off offset:1024 nt
	global_load_dwordx4 v[4:7], v[198:199], off offset:1024 nt
	global_load_dwordx4 v[8:11], v[200:201], off offset:1024 nt
	global_load_dwordx4 v[120:123], v128, s[48:49] nt
	global_load_dwordx4 v[12:15], v[202:203], off offset:1024 nt
	v_readlane_b32 s28, v254, 34
	v_readlane_b32 s29, v254, 35
	v_readlane_b32 s30, v254, 36
	v_readlane_b32 s31, v254, 37
	v_lshl_add_u64 v[140:141], s[50:51], 0, v[130:131]
	s_waitcnt vmcnt(1)
; #define LAS __attribute__((address_space(3)))
; __device__ __forceinline__ unsigned pack4_fp8(float a, float b, float c, float d) { int r = 0; r = __builtin_amdgcn_cvt_pk_fp8_f32(a, b, r, false); r = __builtin_amdgcn_cvt_pk_fp8_f32(c, d, r, true); return (unsigned)r; }
; __device__ __forceinline__ void cvt8_to_lds(const f32x4 (&v)[16], LAS unsigned char* tile, int lane, int wv) {
; #pragma unroll
;     for (int i = 0; i < 4; ++i) { u32x4 w; w.x = pack4_fp8(v[0][i] * W8_SCALE, v[1][i] * W8_SCALE, v[2][i] * W8_SCALE, v[3][i] * W8_SCALE); w.y = pack4_fp8(v[4][i] * W8_SCALE, v[5][i] * W8_SCALE, v[6][i] * W8_SCALE, v[7][i] * W8_SCALE);
;         w.z = pack4_fp8(v[8][i] * W8_SCALE, v[9][i] * W8_SCALE, v[10][i] * W8_SCALE, v[11][i] * W8_SCALE); w.w = pack4_fp8(v[12][i] * W8_SCALE, v[13][i] * W8_SCALE, v[14][i] * W8_SCALE, v[15][i] * W8_SCALE);
;         *(LAS u32x4*)(tile + (4 * lane + i) * 128 + ((wv ^ (lane & 7)) << 4)) = w; }
; }
; __device__ __forceinline__ void cvt8_from_lds(const LAS unsigned char* tile, fp8_t* d, int ld_dst, int tid) {
;     const int c = tid & 7;
; #pragma unroll
;     for (int q = 0; q < 4; ++q) { const int r = (tid >> 3) + 64 * q; const u32x4 w = *(const LAS u32x4*)(tile + r * 128 + ((c ^ ((r >> 2) & 7)) << 4));
;         __builtin_nontemporal_store(w, (u32x4*)(d + (size_t)r * ld_dst + 16 * c)); }
; }
; __device__ __forceinline__ void cvt_item_lds(const float* src, int ld_src, fp8_t* dst, int ld_dst, LAS unsigned char* lds, int tid, int wv) {
;     const int lane = tid & 63;
;     const float* s = src + (size_t)(16 * wv) * ld_src + 4 * lane;
;     f32x4 va[16], vb[16];
;     cvt8_load(va, s, ld_src);
; #pragma unroll
;     for (int t = 0; t < 8; t += 2) {
;         cvt8_load(vb, s + (t + 1) * 256, ld_src); __builtin_amdgcn_sched_barrier(0);
;         cvt8_to_lds(va, lds, lane, wv); CVT_LDS_BAR(); __builtin_amdgcn_sched_barrier(0);
;         cvt8_from_lds(lds, dst + (size_t)(t * 256) * ld_dst, ld_dst, tid); __builtin_amdgcn_sched_barrier(0);
;         if (t + 2 < 8) { cvt8_load(va, s + (t + 2) * 256, ld_src); __builtin_amdgcn_sched_barrier(0); }
;         cvt8_to_lds(vb, lds + 32768, lane, wv); CVT_LDS_BAR(); __builtin_amdgcn_sched_barrier(0);
;         cvt8_from_lds(lds + 32768, dst + (size_t)((t + 1) * 256) * ld_dst, ld_dst, tid); __builtin_amdgcn_sched_barrier(0);
	v_mul_f32_e32 v120, 0x42800000, v120
	v_mul_f32_e32 v116, 0x42800000, v116
	v_mov_b32_e32 v210, v129
	v_cvt_pk_fp8_f32 v210, v120, v116
	v_mul_f32_e32 v16, 0x42800000, v16
	v_mul_f32_e32 v20, 0x42800000, v20
	v_mov_b32_e32 v211, v129
	v_cvt_pk_fp8_f32 v210, v16, v20 op_sel:[0,0,1]
	v_mul_f32_e32 v16, 0x42800000, v24
	v_mul_f32_e32 v20, 0x42800000, v28
	v_cvt_pk_fp8_f32 v211, v16, v20
	v_mul_f32_e32 v16, 0x42800000, v48
	v_mul_f32_e32 v20, 0x42800000, v52
	v_mov_b32_e32 v212, v129
	v_cvt_pk_fp8_f32 v212, v16, v20
	v_mul_f32_e32 v16, 0x42800000, v88
	v_mul_f32_e32 v20, 0x42800000, v92
	v_mov_b32_e32 v213, v129
	v_cvt_pk_fp8_f32 v213, v16, v20
	v_mul_f32_e32 v24, 0x42800000, v56
	v_mul_f32_e32 v28, 0x42800000, v60
	v_cvt_pk_fp8_f32 v211, v24, v28 op_sel:[0,0,1]
	v_mul_f32_e32 v24, 0x42800000, v80
	v_mul_f32_e32 v28, 0x42800000, v84
	v_cvt_pk_fp8_f32 v212, v24, v28 op_sel:[0,0,1]
	v_mul_f32_e32 v24, 0x42800000, v108
	v_mul_f32_e32 v28, 0x42800000, v112
	v_cvt_pk_fp8_f32 v213, v24, v28 op_sel:[0,0,1]
	v_mul_f32_e32 v16, 0x42800000, v121
	v_mul_f32_e32 v20, 0x42800000, v117
	v_mul_f32_e32 v17, 0x42800000, v17
	ds_write_b128 v204, v[210:213]
	v_mov_b32_e32 v210, v129
	v_cvt_pk_fp8_f32 v210, v16, v20
	v_mul_f32_e32 v21, 0x42800000, v21
	v_mul_f32_e32 v16, 0x42800000, v25
	v_mov_b32_e32 v211, v129
	v_cvt_pk_fp8_f32 v210, v17, v21 op_sel:[0,0,1]
	v_mul_f32_e32 v17, 0x42800000, v29
	v_cvt_pk_fp8_f32 v211, v16, v17
	v_mul_f32_e32 v16, 0x42800000, v49
	v_mul_f32_e32 v17, 0x42800000, v53
	v_mov_b32_e32 v212, v129
	v_cvt_pk_fp8_f32 v212, v16, v17
	v_mul_f32_e32 v16, 0x42800000, v89
	v_mul_f32_e32 v17, 0x42800000, v93
	v_mov_b32_e32 v213, v129
	v_cvt_pk_fp8_f32 v213, v16, v17
	v_mul_f32_e32 v20, 0x42800000, v57
	v_mul_f32_e32 v21, 0x42800000, v61
	v_cvt_pk_fp8_f32 v211, v20, v21 op_sel:[0,0,1]
	v_mul_f32_e32 v20, 0x42800000, v81
	v_mul_f32_e32 v21, 0x42800000, v85
	v_cvt_pk_fp8_f32 v212, v20, v21 op_sel:[0,0,1]
	v_mul_f32_e32 v20, 0x42800000, v109
	v_mul_f32_e32 v21, 0x42800000, v113
	v_cvt_pk_fp8_f32 v213, v20, v21 op_sel:[0,0,1]
	v_mul_f32_e32 v16, 0x42800000, v122
	v_mul_f32_e32 v17, 0x42800000, v118
	v_mul_f32_e32 v18, 0x42800000, v18
	ds_write_b128 v204, v[210:213] offset:128
	v_mov_b32_e32 v210, v129
	v_cvt_pk_fp8_f32 v210, v16, v17
	v_mul_f32_e32 v16, 0x42800000, v26
	v_mul_f32_e32 v17, 0x42800000, v30
	v_mov_b32_e32 v211, v129
	v_cvt_pk_fp8_f32 v211, v16, v17
	v_mul_f32_e32 v16, 0x42800000, v50
	v_mul_f32_e32 v17, 0x42800000, v54
	v_mov_b32_e32 v212, v129
	v_cvt_pk_fp8_f32 v212, v16, v17
	v_mul_f32_e32 v16, 0x42800000, v90
	v_mul_f32_e32 v17, 0x42800000, v94
	v_mov_b32_e32 v213, v129
	v_mul_f32_e32 v20, 0x42800000, v22
	v_cvt_pk_fp8_f32 v213, v16, v17
	v_cvt_pk_fp8_f32 v210, v18, v20 op_sel:[0,0,1]
	v_mul_f32_e32 v18, 0x42800000, v58
	v_mul_f32_e32 v20, 0x42800000, v62
	v_cvt_pk_fp8_f32 v211, v18, v20 op_sel:[0,0,1]
	v_mul_f32_e32 v18, 0x42800000, v82
	v_mul_f32_e32 v20, 0x42800000, v86
	v_cvt_pk_fp8_f32 v212, v18, v20 op_sel:[0,0,1]
	v_mul_f32_e32 v18, 0x42800000, v110
	v_mul_f32_e32 v20, 0x42800000, v114
	v_cvt_pk_fp8_f32 v213, v18, v20 op_sel:[0,0,1]
	v_mul_f32_e32 v17, 0x42800000, v123
	v_mul_f32_e32 v18, 0x42800000, v119
	v_mov_b32_e32 v16, v129
	v_cvt_pk_fp8_f32 v16, v17, v18
	v_mul_f32_e32 v19, 0x42800000, v19
	v_mul_f32_e32 v20, 0x42800000, v23
	v_mul_f32_e32 v18, 0x42800000, v27
	v_cvt_pk_fp8_f32 v16, v19, v20 op_sel:[0,0,1]
	v_mul_f32_e32 v19, 0x42800000, v31
	v_mov_b32_e32 v17, v129
	v_cvt_pk_fp8_f32 v17, v18, v19
	v_mul_f32_e32 v20, 0x42800000, v59
	v_mul_f32_e32 v21, 0x42800000, v63
	v_mul_f32_e32 v19, 0x42800000, v51
	v_cvt_pk_fp8_f32 v17, v20, v21 op_sel:[0,0,1]
	v_mul_f32_e32 v20, 0x42800000, v55
	v_mov_b32_e32 v18, v129
	v_cvt_pk_fp8_f32 v18, v19, v20
	v_mul_f32_e32 v21, 0x42800000, v83
	v_mul_f32_e32 v22, 0x42800000, v87
	v_mul_f32_e32 v20, 0x42800000, v91
	v_cvt_pk_fp8_f32 v18, v21, v22 op_sel:[0,0,1]
	v_mul_f32_e32 v21, 0x42800000, v95
	v_mov_b32_e32 v19, v129
	v_cvt_pk_fp8_f32 v19, v20, v21
	v_mul_f32_e32 v22, 0x42800000, v111
	v_mul_f32_e32 v23, 0x42800000, v115
	ds_write_b128 v204, v[210:213] offset:256
	v_cvt_pk_fp8_f32 v19, v22, v23 op_sel:[0,0,1]
	ds_write_b128 v204, v[16:19] offset:384
	s_waitcnt lgkmcnt(0)
	s_barrier
	ds_read_b128 v[16:19], v205
	v_lshl_add_u64 v[20:21], v[140:141], 0, v[132:133]
	s_waitcnt lgkmcnt(0)
	global_store_dwordx4 v[20:21], v[16:19], off nt
	ds_read_b128 v[16:19], v206
	v_lshl_add_u64 v[20:21], v[140:141], 0, v[134:135]
	s_waitcnt lgkmcnt(0)
	global_store_dwordx4 v[20:21], v[16:19], off nt
	ds_read_b128 v[16:19], v207
	v_lshl_add_u64 v[20:21], v[140:141], 0, v[136:137]
	s_waitcnt lgkmcnt(0)
	global_store_dwordx4 v[20:21], v[16:19], off nt
	ds_read_b128 v[16:19], v208
	v_lshl_add_u64 v[20:21], v[140:141], 0, v[138:139]
	s_waitcnt lgkmcnt(0)
; #define LAS __attribute__((address_space(3)))
; __device__ __forceinline__ unsigned pack4_fp8(float a, float b, float c, float d) { int r = 0; r = __builtin_amdgcn_cvt_pk_fp8_f32(a, b, r, false); r = __builtin_amdgcn_cvt_pk_fp8_f32(c, d, r, true); return (unsigned)r; }
; __device__ __forceinline__ void cvt8_to_lds(const f32x4 (&v)[16], LAS unsigned char* tile, int lane, int wv) {
; #pragma unroll
;     for (int i = 0; i < 4; ++i) { u32x4 w; w.x = pack4_fp8(v[0][i] * W8_SCALE, v[1][i] * W8_SCALE, v[2][i] * W8_SCALE, v[3][i] * W8_SCALE); w.y = pack4_fp8(v[4][i] * W8_SCALE, v[5][i] * W8_SCALE, v[6][i] * W8_SCALE, v[7][i] * W8_SCALE);
;         w.z = pack4_fp8(v[8][i] * W8_SCALE, v[9][i] * W8_SCALE, v[10][i] * W8_SCALE, v[11][i] * W8_SCALE); w.w = pack4_fp8(v[12][i] * W8_SCALE, v[13][i] * W8_SCALE, v[14][i] * W8_SCALE, v[15][i] * W8_SCALE);
;         *(LAS u32x4*)(tile + (4 * lane + i) * 128 + ((wv ^ (lane & 7)) << 4)) = w; }
; }
; __device__ __forceinline__ void cvt8_from_lds(const LAS unsigned char* tile, fp8_t* d, int ld_dst, int tid) {
;     const int c = tid & 7;
; #pragma unroll
;     for (int q = 0; q < 4; ++q) { const int r = (tid >> 3) + 64 * q; const u32x4 w = *(const LAS u32x4*)(tile + r * 128 + ((c ^ ((r >> 2) & 7)) << 4));
;         __builtin_nontemporal_store(w, (u32x4*)(d + (size_t)r * ld_dst + 16 * c)); }
; }
; __device__ __forceinline__ void cvt_item_lds(const float* src, int ld_src, fp8_t* dst, int ld_dst, LAS unsigned char* lds, int tid, int wv) {
;     const int lane = tid & 63;
;     const float* s = src + (size_t)(16 * wv) * ld_src + 4 * lane;
;     f32x4 va[16], vb[16];
;     cvt8_load(va, s, ld_src);
; #pragma unroll
;     for (int t = 0; t < 8; t += 2) {
;         cvt8_load(vb, s + (t + 1) * 256, ld_src); __builtin_amdgcn_sched_barrier(0);
;         cvt8_to_lds(va, lds, lane, wv); CVT_LDS_BAR(); __builtin_amdgcn_sched_barrier(0);
;         cvt8_from_lds(lds, dst + (size_t)(t * 256) * ld_dst, ld_dst, tid); __builtin_amdgcn_sched_barrier(0);
;         if (t + 2 < 8) { cvt8_load(va, s + (t + 2) * 256, ld_src); __builtin_amdgcn_sched_barrier(0); }
;         cvt8_to_lds(vb, lds + 32768, lane, wv); CVT_LDS_BAR(); __builtin_amdgcn_sched_barrier(0);
;         cvt8_from_lds(lds + 32768, dst + (size_t)((t + 1) * 256) * ld_dst, ld_dst, tid); __builtin_amdgcn_sched_barrier(0);
	global_store_dwordx4 v[20:21], v[16:19], off nt
	global_load_dwordx4 v[108:111], v[174:175], off offset:2048 nt
	global_load_dwordx4 v[112:115], v[176:177], off offset:2048 nt
	global_load_dwordx4 v[116:119], v[178:179], off offset:2048 nt
	global_load_dwordx4 v[80:83], v[180:181], off offset:2048 nt
	global_load_dwordx4 v[84:87], v[182:183], off offset:2048 nt
	global_load_dwordx4 v[88:91], v[184:185], off offset:2048 nt
	global_load_dwordx4 v[92:95], v[186:187], off offset:2048 nt
	global_load_dwordx4 v[48:51], v[188:189], off offset:2048 nt
	global_load_dwordx4 v[52:55], v[190:191], off offset:2048 nt
	global_load_dwordx4 v[56:59], v[192:193], off offset:2048 nt
	global_load_dwordx4 v[60:63], v[194:195], off offset:2048 nt
	global_load_dwordx4 v[16:19], v[196:197], off offset:2048 nt
	global_load_dwordx4 v[20:23], v[198:199], off offset:2048 nt
	global_load_dwordx4 v[24:27], v[200:201], off offset:2048 nt
	global_load_dwordx4 v[120:123], v128, s[48:49] offset:2048 nt
	global_load_dwordx4 v[28:31], v[202:203], off offset:2048 nt
	v_mul_f32_e32 v96, 0x42800000, v96
	v_mul_f32_e32 v100, 0x42800000, v100
	v_mov_b32_e32 v210, v129
	v_mul_f32_e32 v64, 0x42800000, v64
	v_mul_f32_e32 v68, 0x42800000, v68
	v_mov_b32_e32 v211, v129
	v_mul_f32_e32 v32, 0x42800000, v32
	v_mul_f32_e32 v36, 0x42800000, v36
	v_mov_b32_e32 v212, v129
	v_mul_f32_e32 v0, 0x42800000, v0
	v_mul_f32_e32 v4, 0x42800000, v4
	v_mov_b32_e32 v213, v129
	v_cvt_pk_fp8_f32 v210, v96, v100
	v_cvt_pk_fp8_f32 v211, v64, v68
	v_cvt_pk_fp8_f32 v212, v32, v36
	v_cvt_pk_fp8_f32 v213, v0, v4
	v_mul_f32_e32 v104, 0x42800000, v104
	v_mul_f32_e32 v124, 0x42800000, v124
	v_mul_f32_e32 v72, 0x42800000, v72
	v_mul_f32_e32 v76, 0x42800000, v76
	v_mul_f32_e32 v40, 0x42800000, v40
	v_mul_f32_e32 v44, 0x42800000, v44
	v_mul_f32_e32 v8, 0x42800000, v8
	s_waitcnt vmcnt(20)
	v_mul_f32_e32 v12, 0x42800000, v12
	v_cvt_pk_fp8_f32 v210, v104, v124 op_sel:[0,0,1]
	v_cvt_pk_fp8_f32 v211, v72, v76 op_sel:[0,0,1]
	v_cvt_pk_fp8_f32 v212, v40, v44 op_sel:[0,0,1]
	v_cvt_pk_fp8_f32 v213, v8, v12 op_sel:[0,0,1]
	v_mul_f32_e32 v0, 0x42800000, v97
	v_mul_f32_e32 v4, 0x42800000, v101
	v_mul_f32_e32 v8, 0x42800000, v105
	ds_write_b128 v204, v[210:213] offset:32768
	v_mov_b32_e32 v210, v129
	v_cvt_pk_fp8_f32 v210, v0, v4
	v_mul_f32_e32 v0, 0x42800000, v65
	v_mul_f32_e32 v4, 0x42800000, v69
	v_mov_b32_e32 v211, v129
	v_cvt_pk_fp8_f32 v211, v0, v4
	v_mul_f32_e32 v0, 0x42800000, v33
	v_mul_f32_e32 v4, 0x42800000, v37
	v_mov_b32_e32 v212, v129
	v_cvt_pk_fp8_f32 v212, v0, v4
	v_mul_f32_e32 v0, 0x42800000, v1
	v_mul_f32_e32 v1, 0x42800000, v5
	v_mov_b32_e32 v213, v129
	v_cvt_pk_fp8_f32 v213, v0, v1
	v_mul_f32_e32 v12, 0x42800000, v125
	v_cvt_pk_fp8_f32 v210, v8, v12 op_sel:[0,0,1]
	v_mul_f32_e32 v8, 0x42800000, v73
	v_mul_f32_e32 v12, 0x42800000, v77
	v_cvt_pk_fp8_f32 v211, v8, v12 op_sel:[0,0,1]
	v_mul_f32_e32 v8, 0x42800000, v41
	v_mul_f32_e32 v12, 0x42800000, v45
	v_mul_f32_e32 v4, 0x42800000, v9
	v_mul_f32_e32 v5, 0x42800000, v13
	v_cvt_pk_fp8_f32 v212, v8, v12 op_sel:[0,0,1]
	v_cvt_pk_fp8_f32 v213, v4, v5 op_sel:[0,0,1]
	v_mul_f32_e32 v0, 0x42800000, v98
	v_mul_f32_e32 v1, 0x42800000, v102
	v_mul_f32_e32 v4, 0x42800000, v106
	ds_write_b128 v204, v[210:213] offset:32896
	v_mov_b32_e32 v210, v129
	v_cvt_pk_fp8_f32 v210, v0, v1
	v_mul_f32_e32 v0, 0x42800000, v66
	v_mul_f32_e32 v1, 0x42800000, v70
	v_mov_b32_e32 v211, v129
	v_cvt_pk_fp8_f32 v211, v0, v1
	v_mul_f32_e32 v0, 0x42800000, v34
	v_mul_f32_e32 v1, 0x42800000, v38
	v_mov_b32_e32 v212, v129
	v_cvt_pk_fp8_f32 v212, v0, v1
	v_mul_f32_e32 v0, 0x42800000, v2
	v_mul_f32_e32 v1, 0x42800000, v6
	v_mov_b32_e32 v213, v129
	v_mul_f32_e32 v5, 0x42800000, v126
	v_cvt_pk_fp8_f32 v213, v0, v1
	v_cvt_pk_fp8_f32 v210, v4, v5 op_sel:[0,0,1]
	v_mul_f32_e32 v4, 0x42800000, v74
	v_mul_f32_e32 v5, 0x42800000, v78
	v_cvt_pk_fp8_f32 v211, v4, v5 op_sel:[0,0,1]
	v_mul_f32_e32 v4, 0x42800000, v42
	v_mul_f32_e32 v5, 0x42800000, v46
	v_cvt_pk_fp8_f32 v212, v4, v5 op_sel:[0,0,1]
	v_mul_f32_e32 v2, 0x42800000, v10
	v_mul_f32_e32 v4, 0x42800000, v14
	v_cvt_pk_fp8_f32 v213, v2, v4 op_sel:[0,0,1]
	v_mul_f32_e32 v1, 0x42800000, v99
	v_mul_f32_e32 v2, 0x42800000, v103
	v_mov_b32_e32 v0, v129
	v_cvt_pk_fp8_f32 v0, v1, v2
	v_mul_f32_e32 v4, 0x42800000, v107
	v_mul_f32_e32 v5, 0x42800000, v127
	v_mul_f32_e32 v2, 0x42800000, v67
	v_cvt_pk_fp8_f32 v0, v4, v5 op_sel:[0,0,1]
	v_mul_f32_e32 v4, 0x42800000, v71
	v_mov_b32_e32 v1, v129
	v_cvt_pk_fp8_f32 v1, v2, v4
	v_mul_f32_e32 v5, 0x42800000, v75
	v_mul_f32_e32 v6, 0x42800000, v79
	v_mul_f32_e32 v4, 0x42800000, v35
	v_cvt_pk_fp8_f32 v1, v5, v6 op_sel:[0,0,1]
	v_mul_f32_e32 v5, 0x42800000, v39
	v_mov_b32_e32 v2, v129
	v_cvt_pk_fp8_f32 v2, v4, v5
	v_mul_f32_e32 v4, 0x42800000, v3
	v_mul_f32_e32 v5, 0x42800000, v7
	v_mov_b32_e32 v3, v129
	v_cvt_pk_fp8_f32 v3, v4, v5
	v_mul_f32_e32 v6, 0x42800000, v43
	v_mul_f32_e32 v8, 0x42800000, v47
	v_cvt_pk_fp8_f32 v2, v6, v8 op_sel:[0,0,1]
	v_mul_f32_e32 v6, 0x42800000, v11
	v_mul_f32_e32 v7, 0x42800000, v15
	v_cvt_pk_fp8_f32 v3, v6, v7 op_sel:[0,0,1]
	ds_write_b128 v204, v[210:213] offset:33024
	ds_write_b128 v204, v[0:3] offset:33152
	s_waitcnt lgkmcnt(0)
	s_barrier
; #define LAS __attribute__((address_space(3)))
; __device__ __forceinline__ unsigned pack4_fp8(float a, float b, float c, float d) { int r = 0; r = __builtin_amdgcn_cvt_pk_fp8_f32(a, b, r, false); r = __builtin_amdgcn_cvt_pk_fp8_f32(c, d, r, true); return (unsigned)r; }
; __device__ __forceinline__ void cvt8_to_lds(const f32x4 (&v)[16], LAS unsigned char* tile, int lane, int wv) {
; #pragma unroll
;     for (int i = 0; i < 4; ++i) { u32x4 w; w.x = pack4_fp8(v[0][i] * W8_SCALE, v[1][i] * W8_SCALE, v[2][i] * W8_SCALE, v[3][i] * W8_SCALE); w.y = pack4_fp8(v[4][i] * W8_SCALE, v[5][i] * W8_SCALE, v[6][i] * W8_SCALE, v[7][i] * W8_SCALE);
;         w.z = pack4_fp8(v[8][i] * W8_SCALE, v[9][i] * W8_SCALE, v[10][i] * W8_SCALE, v[11][i] * W8_SCALE); w.w = pack4_fp8(v[12][i] * W8_SCALE, v[13][i] * W8_SCALE, v[14][i] * W8_SCALE, v[15][i] * W8_SCALE);
;         *(LAS u32x4*)(tile + (4 * lane + i) * 128 + ((wv ^ (lane & 7)) << 4)) = w; }
; }
; __device__ __forceinline__ void cvt8_from_lds(const LAS unsigned char* tile, fp8_t* d, int ld_dst, int tid) {
;     const int c = tid & 7;
; #pragma unroll
;     for (int q = 0; q < 4; ++q) { const int r = (tid >> 3) + 64 * q; const u32x4 w = *(const LAS u32x4*)(tile + r * 128 + ((c ^ ((r >> 2) & 7)) << 4));
;         __builtin_nontemporal_store(w, (u32x4*)(d + (size_t)r * ld_dst + 16 * c)); }
; }
; __device__ __forceinline__ void cvt_item_lds(const float* src, int ld_src, fp8_t* dst, int ld_dst, LAS unsigned char* lds, int tid, int wv) {
;     const int lane = tid & 63;
;     const float* s = src + (size_t)(16 * wv) * ld_src + 4 * lane;
;     f32x4 va[16], vb[16];
;     cvt8_load(va, s, ld_src);
; #pragma unroll
;     for (int t = 0; t < 8; t += 2) {
;         cvt8_load(vb, s + (t + 1) * 256, ld_src); __builtin_amdgcn_sched_barrier(0);
;         cvt8_to_lds(va, lds, lane, wv); CVT_LDS_BAR(); __builtin_amdgcn_sched_barrier(0);
;         cvt8_from_lds(lds, dst + (size_t)(t * 256) * ld_dst, ld_dst, tid); __builtin_amdgcn_sched_barrier(0);
;         if (t + 2 < 8) { cvt8_load(va, s + (t + 2) * 256, ld_src); __builtin_amdgcn_sched_barrier(0); }
;         cvt8_to_lds(vb, lds + 32768, lane, wv); CVT_LDS_BAR(); __builtin_amdgcn_sched_barrier(0);
;         cvt8_from_lds(lds + 32768, dst + (size_t)((t + 1) * 256) * ld_dst, ld_dst, tid); __builtin_amdgcn_sched_barrier(0);
	ds_read_b128 v[0:3], v205 offset:32768
	v_lshl_add_u64 v[4:5], v[140:141], 0, s[8:9]
	v_lshl_add_u64 v[6:7], v[4:5], 0, v[132:133]
	s_waitcnt lgkmcnt(0)
	global_store_dwordx4 v[6:7], v[0:3], off nt
	ds_read_b128 v[0:3], v206 offset:32768
	v_lshl_add_u64 v[6:7], v[4:5], 0, v[134:135]
	s_waitcnt lgkmcnt(0)
	global_store_dwordx4 v[6:7], v[0:3], off nt
	ds_read_b128 v[0:3], v207 offset:32768
	v_lshl_add_u64 v[6:7], v[4:5], 0, v[136:137]
	v_lshl_add_u64 v[4:5], v[4:5], 0, v[138:139]
	s_waitcnt lgkmcnt(0)
	global_store_dwordx4 v[6:7], v[0:3], off nt
	ds_read_b128 v[0:3], v208 offset:32768
	s_waitcnt lgkmcnt(0)
	global_store_dwordx4 v[4:5], v[0:3], off nt
	global_load_dwordx4 v[96:99], v[174:175], off offset:3072 nt
	global_load_dwordx4 v[100:103], v[176:177], off offset:3072 nt
	global_load_dwordx4 v[104:107], v[178:179], off offset:3072 nt
	global_load_dwordx4 v[64:67], v[180:181], off offset:3072 nt
	global_load_dwordx4 v[68:71], v[182:183], off offset:3072 nt
	global_load_dwordx4 v[72:75], v[184:185], off offset:3072 nt
	global_load_dwordx4 v[76:79], v[186:187], off offset:3072 nt
	global_load_dwordx4 v[32:35], v[188:189], off offset:3072 nt
	global_load_dwordx4 v[36:39], v[190:191], off offset:3072 nt
	global_load_dwordx4 v[40:43], v[192:193], off offset:3072 nt
	global_load_dwordx4 v[44:47], v[194:195], off offset:3072 nt
	global_load_dwordx4 v[0:3], v[196:197], off offset:3072 nt
	global_load_dwordx4 v[4:7], v[198:199], off offset:3072 nt
	global_load_dwordx4 v[8:11], v[200:201], off offset:3072 nt
	global_load_dwordx4 v[124:127], v128, s[48:49] offset:3072 nt
	global_load_dwordx4 v[12:15], v[202:203], off offset:3072 nt
	s_waitcnt vmcnt(21)
	v_mul_f32_e32 v120, 0x42800000, v120
	v_mul_f32_e32 v108, 0x42800000, v108
	v_mov_b32_e32 v174, v129
	v_mul_f32_e32 v80, 0x42800000, v80
	v_mul_f32_e32 v84, 0x42800000, v84
	v_mov_b32_e32 v175, v129
	v_mul_f32_e32 v48, 0x42800000, v48
	v_mul_f32_e32 v52, 0x42800000, v52
	v_mov_b32_e32 v176, v129
	v_mul_f32_e32 v16, 0x42800000, v16
	v_mul_f32_e32 v20, 0x42800000, v20
	v_mov_b32_e32 v177, v129
	v_cvt_pk_fp8_f32 v174, v120, v108
	v_cvt_pk_fp8_f32 v175, v80, v84
	v_cvt_pk_fp8_f32 v176, v48, v52
	v_cvt_pk_fp8_f32 v177, v16, v20
	v_mul_f32_e32 v112, 0x42800000, v112
	v_mul_f32_e32 v116, 0x42800000, v116
	v_mul_f32_e32 v88, 0x42800000, v88
	v_mul_f32_e32 v92, 0x42800000, v92
	v_mul_f32_e32 v56, 0x42800000, v56
	v_mul_f32_e32 v60, 0x42800000, v60
	v_mul_f32_e32 v24, 0x42800000, v24
	s_waitcnt vmcnt(20)
	v_mul_f32_e32 v28, 0x42800000, v28
	v_cvt_pk_fp8_f32 v174, v112, v116 op_sel:[0,0,1]
	v_cvt_pk_fp8_f32 v175, v88, v92 op_sel:[0,0,1]
	v_cvt_pk_fp8_f32 v176, v56, v60 op_sel:[0,0,1]
	v_cvt_pk_fp8_f32 v177, v24, v28 op_sel:[0,0,1]
	v_mul_f32_e32 v16, 0x42800000, v121
	v_mul_f32_e32 v20, 0x42800000, v109
	v_mul_f32_e32 v24, 0x42800000, v113
	ds_write_b128 v204, v[174:177]
	v_mov_b32_e32 v174, v129
	v_cvt_pk_fp8_f32 v174, v16, v20
	v_mul_f32_e32 v16, 0x42800000, v81
	v_mul_f32_e32 v20, 0x42800000, v85
	v_mov_b32_e32 v175, v129
	v_cvt_pk_fp8_f32 v175, v16, v20
	v_mul_f32_e32 v16, 0x42800000, v49
	v_mul_f32_e32 v20, 0x42800000, v53
	v_mov_b32_e32 v176, v129
	v_cvt_pk_fp8_f32 v176, v16, v20
	v_mul_f32_e32 v16, 0x42800000, v17
	v_mul_f32_e32 v17, 0x42800000, v21
	v_mov_b32_e32 v177, v129
	v_cvt_pk_fp8_f32 v177, v16, v17
	v_mul_f32_e32 v28, 0x42800000, v117
	v_cvt_pk_fp8_f32 v174, v24, v28 op_sel:[0,0,1]
	v_mul_f32_e32 v24, 0x42800000, v89
	v_mul_f32_e32 v28, 0x42800000, v93
	v_cvt_pk_fp8_f32 v175, v24, v28 op_sel:[0,0,1]
	v_mul_f32_e32 v24, 0x42800000, v57
	v_mul_f32_e32 v28, 0x42800000, v61
	v_mul_f32_e32 v20, 0x42800000, v25
	v_mul_f32_e32 v21, 0x42800000, v29
	v_cvt_pk_fp8_f32 v176, v24, v28 op_sel:[0,0,1]
	v_cvt_pk_fp8_f32 v177, v20, v21 op_sel:[0,0,1]
	v_mul_f32_e32 v16, 0x42800000, v122
	v_mul_f32_e32 v17, 0x42800000, v110
	v_mul_f32_e32 v20, 0x42800000, v114
	ds_write_b128 v204, v[174:177] offset:128
	v_mov_b32_e32 v174, v129
	v_cvt_pk_fp8_f32 v174, v16, v17
	v_mul_f32_e32 v16, 0x42800000, v82
	v_mul_f32_e32 v17, 0x42800000, v86
	v_mov_b32_e32 v175, v129
	v_cvt_pk_fp8_f32 v175, v16, v17
	v_mul_f32_e32 v16, 0x42800000, v50
	v_mul_f32_e32 v17, 0x42800000, v54
	v_mov_b32_e32 v176, v129
	v_cvt_pk_fp8_f32 v176, v16, v17
	v_mul_f32_e32 v16, 0x42800000, v18
	v_mul_f32_e32 v17, 0x42800000, v22
	v_mov_b32_e32 v177, v129
	v_mul_f32_e32 v21, 0x42800000, v118
	v_cvt_pk_fp8_f32 v177, v16, v17
	v_cvt_pk_fp8_f32 v174, v20, v21 op_sel:[0,0,1]
	v_mul_f32_e32 v20, 0x42800000, v90
	v_mul_f32_e32 v21, 0x42800000, v94
	v_cvt_pk_fp8_f32 v175, v20, v21 op_sel:[0,0,1]
	v_mul_f32_e32 v20, 0x42800000, v58
	v_mul_f32_e32 v21, 0x42800000, v62
	v_cvt_pk_fp8_f32 v176, v20, v21 op_sel:[0,0,1]
	v_mul_f32_e32 v18, 0x42800000, v26
	v_mul_f32_e32 v20, 0x42800000, v30
	v_cvt_pk_fp8_f32 v177, v18, v20 op_sel:[0,0,1]
	v_mul_f32_e32 v17, 0x42800000, v123
	v_mul_f32_e32 v18, 0x42800000, v111
	v_mov_b32_e32 v16, v129
	v_cvt_pk_fp8_f32 v16, v17, v18
	v_mul_f32_e32 v20, 0x42800000, v115
	v_mul_f32_e32 v21, 0x42800000, v119
	v_mul_f32_e32 v18, 0x42800000, v83
	v_cvt_pk_fp8_f32 v16, v20, v21 op_sel:[0,0,1]
	v_mul_f32_e32 v20, 0x42800000, v87
	v_mov_b32_e32 v17, v129
	v_cvt_pk_fp8_f32 v17, v18, v20
	v_mul_f32_e32 v21, 0x42800000, v91
	v_mul_f32_e32 v22, 0x42800000, v95
	v_mul_f32_e32 v20, 0x42800000, v51
	v_cvt_pk_fp8_f32 v17, v21, v22 op_sel:[0,0,1]
	v_mul_f32_e32 v21, 0x42800000, v55
	v_mov_b32_e32 v18, v129
	v_cvt_pk_fp8_f32 v18, v20, v21
	v_mul_f32_e32 v20, 0x42800000, v19
	v_mul_f32_e32 v21, 0x42800000, v23
	v_mov_b32_e32 v19, v129
	v_cvt_pk_fp8_f32 v19, v20, v21
	v_mul_f32_e32 v22, 0x42800000, v59
	v_mul_f32_e32 v24, 0x42800000, v63
	v_cvt_pk_fp8_f32 v18, v22, v24 op_sel:[0,0,1]
	v_mul_f32_e32 v22, 0x42800000, v27
	v_mul_f32_e32 v23, 0x42800000, v31
	v_cvt_pk_fp8_f32 v19, v22, v23 op_sel:[0,0,1]
	ds_write_b128 v204, v[174:177] offset:256
	ds_write_b128 v204, v[16:19] offset:384
	s_waitcnt lgkmcnt(0)
	s_barrier
; #define LAS __attribute__((address_space(3)))
; __device__ __forceinline__ unsigned pack4_fp8(float a, float b, float c, float d) { int r = 0; r = __builtin_amdgcn_cvt_pk_fp8_f32(a, b, r, false); r = __builtin_amdgcn_cvt_pk_fp8_f32(c, d, r, true); return (unsigned)r; }
; __device__ __forceinline__ void cvt8_to_lds(const f32x4 (&v)[16], LAS unsigned char* tile, int lane, int wv) {
; #pragma unroll
;     for (int i = 0; i < 4; ++i) { u32x4 w; w.x = pack4_fp8(v[0][i] * W8_SCALE, v[1][i] * W8_SCALE, v[2][i] * W8_SCALE, v[3][i] * W8_SCALE); w.y = pack4_fp8(v[4][i] * W8_SCALE, v[5][i] * W8_SCALE, v[6][i] * W8_SCALE, v[7][i] * W8_SCALE);
;         w.z = pack4_fp8(v[8][i] * W8_SCALE, v[9][i] * W8_SCALE, v[10][i] * W8_SCALE, v[11][i] * W8_SCALE); w.w = pack4_fp8(v[12][i] * W8_SCALE, v[13][i] * W8_SCALE, v[14][i] * W8_SCALE, v[15][i] * W8_SCALE);
;         *(LAS u32x4*)(tile + (4 * lane + i) * 128 + ((wv ^ (lane & 7)) << 4)) = w; }
; }
; __device__ __forceinline__ void cvt8_from_lds(const LAS unsigned char* tile, fp8_t* d, int ld_dst, int tid) {
;     const int c = tid & 7;
; #pragma unroll
;     for (int q = 0; q < 4; ++q) { const int r = (tid >> 3) + 64 * q; const u32x4 w = *(const LAS u32x4*)(tile + r * 128 + ((c ^ ((r >> 2) & 7)) << 4));
;         __builtin_nontemporal_store(w, (u32x4*)(d + (size_t)r * ld_dst + 16 * c)); }
; }
; __device__ __forceinline__ void cvt_item_lds(const float* src, int ld_src, fp8_t* dst, int ld_dst, LAS unsigned char* lds, int tid, int wv) {
;     const int lane = tid & 63;
;     const float* s = src + (size_t)(16 * wv) * ld_src + 4 * lane;
;     f32x4 va[16], vb[16];
;     cvt8_load(va, s, ld_src);
; #pragma unroll
;     for (int t = 0; t < 8; t += 2) {
;         cvt8_load(vb, s + (t + 1) * 256, ld_src); __builtin_amdgcn_sched_barrier(0);
;         cvt8_to_lds(va, lds, lane, wv); CVT_LDS_BAR(); __builtin_amdgcn_sched_barrier(0);
;         cvt8_from_lds(lds, dst + (size_t)(t * 256) * ld_dst, ld_dst, tid); __builtin_amdgcn_sched_barrier(0);
;         if (t + 2 < 8) { cvt8_load(va, s + (t + 2) * 256, ld_src); __builtin_amdgcn_sched_barrier(0); }
;         cvt8_to_lds(vb, lds + 32768, lane, wv); CVT_LDS_BAR(); __builtin_amdgcn_sched_barrier(0);
;         cvt8_from_lds(lds + 32768, dst + (size_t)((t + 1) * 256) * ld_dst, ld_dst, tid); __builtin_amdgcn_sched_barrier(0);
	ds_read_b128 v[16:19], v205
	v_lshl_add_u64 v[20:21], v[140:141], 0, s[10:11]
	v_lshl_add_u64 v[22:23], v[20:21], 0, v[132:133]
	s_waitcnt lgkmcnt(0)
	global_store_dwordx4 v[22:23], v[16:19], off nt
	ds_read_b128 v[16:19], v206
	v_lshl_add_u64 v[22:23], v[20:21], 0, v[134:135]
	s_waitcnt lgkmcnt(0)
	global_store_dwordx4 v[22:23], v[16:19], off nt
	ds_read_b128 v[16:19], v207
	v_lshl_add_u64 v[22:23], v[20:21], 0, v[136:137]
	v_lshl_add_u64 v[20:21], v[20:21], 0, v[138:139]
	s_waitcnt lgkmcnt(0)
	global_store_dwordx4 v[22:23], v[16:19], off nt
	ds_read_b128 v[16:19], v208
	s_waitcnt lgkmcnt(0)
	global_store_dwordx4 v[20:21], v[16:19], off nt
	v_add_co_u32_e32 v172, vcc, s66, v172
	s_nop 1
	v_addc_co_u32_e32 v173, vcc, 0, v173, vcc
	global_load_dwordx4 v[108:111], v[172:173], off nt
	global_load_dwordx4 v[112:115], v[142:143], off nt
	global_load_dwordx4 v[116:119], v[144:145], off nt
	global_load_dwordx4 v[120:123], v[146:147], off nt
	global_load_dwordx4 v[80:83], v[148:149], off nt
	global_load_dwordx4 v[84:87], v[150:151], off nt
	global_load_dwordx4 v[88:91], v[152:153], off nt
	global_load_dwordx4 v[92:95], v[154:155], off nt
	global_load_dwordx4 v[48:51], v[156:157], off nt
	global_load_dwordx4 v[52:55], v[158:159], off nt
	global_load_dwordx4 v[56:59], v[160:161], off nt
	global_load_dwordx4 v[60:63], v[162:163], off nt
	global_load_dwordx4 v[16:19], v[164:165], off nt
	global_load_dwordx4 v[20:23], v[166:167], off nt
	global_load_dwordx4 v[24:27], v[168:169], off nt
	global_load_dwordx4 v[28:31], v[170:171], off nt
	s_waitcnt vmcnt(21)
	v_mul_f32_e32 v124, 0x42800000, v124
	v_mul_f32_e32 v96, 0x42800000, v96
	v_mov_b32_e32 v174, v129
	v_mul_f32_e32 v64, 0x42800000, v64
	v_mul_f32_e32 v68, 0x42800000, v68
	v_mov_b32_e32 v175, v129
	v_mul_f32_e32 v32, 0x42800000, v32
	v_mul_f32_e32 v36, 0x42800000, v36
	v_mov_b32_e32 v176, v129
	v_mul_f32_e32 v0, 0x42800000, v0
	v_mul_f32_e32 v4, 0x42800000, v4
	v_mov_b32_e32 v177, v129
	v_cvt_pk_fp8_f32 v174, v124, v96
	v_cvt_pk_fp8_f32 v175, v64, v68
	v_cvt_pk_fp8_f32 v176, v32, v36
	v_cvt_pk_fp8_f32 v177, v0, v4
	v_mul_f32_e32 v100, 0x42800000, v100
	v_mul_f32_e32 v104, 0x42800000, v104
	v_mul_f32_e32 v72, 0x42800000, v72
	v_mul_f32_e32 v76, 0x42800000, v76
	v_mul_f32_e32 v40, 0x42800000, v40
	v_mul_f32_e32 v44, 0x42800000, v44
	v_mul_f32_e32 v8, 0x42800000, v8
	s_waitcnt vmcnt(20)
	v_mul_f32_e32 v12, 0x42800000, v12
	v_cvt_pk_fp8_f32 v174, v100, v104 op_sel:[0,0,1]
	v_cvt_pk_fp8_f32 v175, v72, v76 op_sel:[0,0,1]
	v_cvt_pk_fp8_f32 v176, v40, v44 op_sel:[0,0,1]
	v_cvt_pk_fp8_f32 v177, v8, v12 op_sel:[0,0,1]
	v_mul_f32_e32 v0, 0x42800000, v125
	v_mul_f32_e32 v4, 0x42800000, v97
	v_mul_f32_e32 v8, 0x42800000, v101
	ds_write_b128 v204, v[174:177] offset:32768
	v_mov_b32_e32 v174, v129
	v_cvt_pk_fp8_f32 v174, v0, v4
	v_mul_f32_e32 v0, 0x42800000, v65
	v_mul_f32_e32 v4, 0x42800000, v69
	v_mov_b32_e32 v175, v129
	v_cvt_pk_fp8_f32 v175, v0, v4
	v_mul_f32_e32 v0, 0x42800000, v33
	v_mul_f32_e32 v4, 0x42800000, v37
	v_mov_b32_e32 v176, v129
	v_cvt_pk_fp8_f32 v176, v0, v4
	v_mul_f32_e32 v0, 0x42800000, v1
	v_mul_f32_e32 v1, 0x42800000, v5
	v_mov_b32_e32 v177, v129
	v_cvt_pk_fp8_f32 v177, v0, v1
	v_mul_f32_e32 v12, 0x42800000, v105
	v_cvt_pk_fp8_f32 v174, v8, v12 op_sel:[0,0,1]
	v_mul_f32_e32 v8, 0x42800000, v73
	v_mul_f32_e32 v12, 0x42800000, v77
	v_cvt_pk_fp8_f32 v175, v8, v12 op_sel:[0,0,1]
	v_mul_f32_e32 v8, 0x42800000, v41
	v_mul_f32_e32 v12, 0x42800000, v45
	v_mul_f32_e32 v4, 0x42800000, v9
	v_mul_f32_e32 v5, 0x42800000, v13
	v_cvt_pk_fp8_f32 v176, v8, v12 op_sel:[0,0,1]
	v_cvt_pk_fp8_f32 v177, v4, v5 op_sel:[0,0,1]
	v_mul_f32_e32 v0, 0x42800000, v126
	v_mul_f32_e32 v1, 0x42800000, v98
	v_mul_f32_e32 v4, 0x42800000, v102
	ds_write_b128 v204, v[174:177] offset:32896
	v_mov_b32_e32 v174, v129
	v_cvt_pk_fp8_f32 v174, v0, v1
	v_mul_f32_e32 v0, 0x42800000, v66
	v_mul_f32_e32 v1, 0x42800000, v70
	v_mov_b32_e32 v175, v129
	v_cvt_pk_fp8_f32 v175, v0, v1
	v_mul_f32_e32 v0, 0x42800000, v34
	v_mul_f32_e32 v1, 0x42800000, v38
	v_mov_b32_e32 v176, v129
	v_cvt_pk_fp8_f32 v176, v0, v1
	v_mul_f32_e32 v0, 0x42800000, v2
	v_mul_f32_e32 v1, 0x42800000, v6
	v_mov_b32_e32 v177, v129
	v_mul_f32_e32 v5, 0x42800000, v106
	v_cvt_pk_fp8_f32 v177, v0, v1
	v_cvt_pk_fp8_f32 v174, v4, v5 op_sel:[0,0,1]
	v_mul_f32_e32 v4, 0x42800000, v74
	v_mul_f32_e32 v5, 0x42800000, v78
	v_cvt_pk_fp8_f32 v175, v4, v5 op_sel:[0,0,1]
	v_mul_f32_e32 v4, 0x42800000, v42
	v_mul_f32_e32 v5, 0x42800000, v46
	v_cvt_pk_fp8_f32 v176, v4, v5 op_sel:[0,0,1]
	v_mul_f32_e32 v2, 0x42800000, v10
	v_mul_f32_e32 v4, 0x42800000, v14
	v_cvt_pk_fp8_f32 v177, v2, v4 op_sel:[0,0,1]
	v_mul_f32_e32 v1, 0x42800000, v127
	v_mul_f32_e32 v2, 0x42800000, v99
	v_mov_b32_e32 v0, v129
	v_cvt_pk_fp8_f32 v0, v1, v2
	v_mul_f32_e32 v4, 0x42800000, v103
	v_mul_f32_e32 v5, 0x42800000, v107
	v_mul_f32_e32 v2, 0x42800000, v67
	v_cvt_pk_fp8_f32 v0, v4, v5 op_sel:[0,0,1]
	v_mul_f32_e32 v4, 0x42800000, v71
	v_mov_b32_e32 v1, v129
	v_cvt_pk_fp8_f32 v1, v2, v4
	v_mul_f32_e32 v5, 0x42800000, v75
	v_mul_f32_e32 v6, 0x42800000, v79
	v_mul_f32_e32 v4, 0x42800000, v35
	v_cvt_pk_fp8_f32 v1, v5, v6 op_sel:[0,0,1]
	v_mul_f32_e32 v5, 0x42800000, v39
	v_mov_b32_e32 v2, v129
	v_cvt_pk_fp8_f32 v2, v4, v5
	v_mul_f32_e32 v4, 0x42800000, v3
	v_mul_f32_e32 v5, 0x42800000, v7
	v_mov_b32_e32 v3, v129
	v_cvt_pk_fp8_f32 v3, v4, v5
	v_mul_f32_e32 v6, 0x42800000, v43
	v_mul_f32_e32 v8, 0x42800000, v47
	v_cvt_pk_fp8_f32 v2, v6, v8 op_sel:[0,0,1]
	v_mul_f32_e32 v6, 0x42800000, v11
	v_mul_f32_e32 v7, 0x42800000, v15
	v_cvt_pk_fp8_f32 v3, v6, v7 op_sel:[0,0,1]
	ds_write_b128 v204, v[174:177] offset:33024
	ds_write_b128 v204, v[0:3] offset:33152
	s_waitcnt lgkmcnt(0)
	s_barrier
; #define LAS __attribute__((address_space(3)))
; __device__ __forceinline__ unsigned pack4_fp8(float a, float b, float c, float d) { int r = 0; r = __builtin_amdgcn_cvt_pk_fp8_f32(a, b, r, false); r = __builtin_amdgcn_cvt_pk_fp8_f32(c, d, r, true); return (unsigned)r; }
; __device__ __forceinline__ void cvt8_to_lds(const f32x4 (&v)[16], LAS unsigned char* tile, int lane, int wv) {
; #pragma unroll
;     for (int i = 0; i < 4; ++i) { u32x4 w; w.x = pack4_fp8(v[0][i] * W8_SCALE, v[1][i] * W8_SCALE, v[2][i] * W8_SCALE, v[3][i] * W8_SCALE); w.y = pack4_fp8(v[4][i] * W8_SCALE, v[5][i] * W8_SCALE, v[6][i] * W8_SCALE, v[7][i] * W8_SCALE);
;         w.z = pack4_fp8(v[8][i] * W8_SCALE, v[9][i] * W8_SCALE, v[10][i] * W8_SCALE, v[11][i] * W8_SCALE); w.w = pack4_fp8(v[12][i] * W8_SCALE, v[13][i] * W8_SCALE, v[14][i] * W8_SCALE, v[15][i] * W8_SCALE);
;         *(LAS u32x4*)(tile + (4 * lane + i) * 128 + ((wv ^ (lane & 7)) << 4)) = w; }
; }
; __device__ __forceinline__ void cvt8_from_lds(const LAS unsigned char* tile, fp8_t* d, int ld_dst, int tid) {
;     const int c = tid & 7;
; #pragma unroll
;     for (int q = 0; q < 4; ++q) { const int r = (tid >> 3) + 64 * q; const u32x4 w = *(const LAS u32x4*)(tile + r * 128 + ((c ^ ((r >> 2) & 7)) << 4));
;         __builtin_nontemporal_store(w, (u32x4*)(d + (size_t)r * ld_dst + 16 * c)); }
; }
; __device__ __forceinline__ void cvt_item_lds(const float* src, int ld_src, fp8_t* dst, int ld_dst, LAS unsigned char* lds, int tid, int wv) {
;     const int lane = tid & 63;
;     const float* s = src + (size_t)(16 * wv) * ld_src + 4 * lane;
;     f32x4 va[16], vb[16];
;     cvt8_load(va, s, ld_src);
; #pragma unroll
;     for (int t = 0; t < 8; t += 2) {
;         cvt8_load(vb, s + (t + 1) * 256, ld_src); __builtin_amdgcn_sched_barrier(0);
;         cvt8_to_lds(va, lds, lane, wv); CVT_LDS_BAR(); __builtin_amdgcn_sched_barrier(0);
;         cvt8_from_lds(lds, dst + (size_t)(t * 256) * ld_dst, ld_dst, tid); __builtin_amdgcn_sched_barrier(0);
;         if (t + 2 < 8) { cvt8_load(va, s + (t + 2) * 256, ld_src); __builtin_amdgcn_sched_barrier(0); }
;         cvt8_to_lds(vb, lds + 32768, lane, wv); CVT_LDS_BAR(); __builtin_amdgcn_sched_barrier(0);
;         cvt8_from_lds(lds + 32768, dst + (size_t)((t + 1) * 256) * ld_dst, ld_dst, tid); __builtin_amdgcn_sched_barrier(0);
	ds_read_b128 v[0:3], v205 offset:32768
	v_lshl_add_u64 v[4:5], v[140:141], 0, s[38:39]
	v_lshl_add_u64 v[6:7], v[4:5], 0, v[132:133]
	s_waitcnt lgkmcnt(0)
	global_store_dwordx4 v[6:7], v[0:3], off nt
	ds_read_b128 v[0:3], v206 offset:32768
	v_lshl_add_u64 v[6:7], v[4:5], 0, v[134:135]
	s_waitcnt lgkmcnt(0)
	global_store_dwordx4 v[6:7], v[0:3], off nt
	ds_read_b128 v[0:3], v207 offset:32768
	v_lshl_add_u64 v[6:7], v[4:5], 0, v[136:137]
	v_lshl_add_u64 v[4:5], v[4:5], 0, v[138:139]
	s_waitcnt lgkmcnt(0)
	global_store_dwordx4 v[6:7], v[0:3], off nt
	ds_read_b128 v[0:3], v208 offset:32768
	s_waitcnt lgkmcnt(0)
	global_store_dwordx4 v[4:5], v[0:3], off nt
	global_load_dwordx4 v[96:99], v[172:173], off offset:1024 nt
	global_load_dwordx4 v[100:103], v[142:143], off offset:1024 nt
	global_load_dwordx4 v[104:107], v[144:145], off offset:1024 nt
	global_load_dwordx4 v[124:127], v[146:147], off offset:1024 nt
	global_load_dwordx4 v[64:67], v[148:149], off offset:1024 nt
	global_load_dwordx4 v[68:71], v[150:151], off offset:1024 nt
	global_load_dwordx4 v[72:75], v[152:153], off offset:1024 nt
	global_load_dwordx4 v[76:79], v[154:155], off offset:1024 nt
	global_load_dwordx4 v[32:35], v[156:157], off offset:1024 nt
	global_load_dwordx4 v[36:39], v[158:159], off offset:1024 nt
	global_load_dwordx4 v[40:43], v[160:161], off offset:1024 nt
	global_load_dwordx4 v[44:47], v[162:163], off offset:1024 nt
	global_load_dwordx4 v[0:3], v[164:165], off offset:1024 nt
	global_load_dwordx4 v[4:7], v[166:167], off offset:1024 nt
	global_load_dwordx4 v[8:11], v[168:169], off offset:1024 nt
	global_load_dwordx4 v[12:15], v[170:171], off offset:1024 nt
	s_waitcnt vmcnt(35)
	v_mul_f32_e32 v108, 0x42800000, v108
	s_waitcnt vmcnt(34)
	v_mul_f32_e32 v112, 0x42800000, v112
	v_mov_b32_e32 v174, v129
	s_waitcnt vmcnt(31)
	v_mul_f32_e32 v80, 0x42800000, v80
	s_waitcnt vmcnt(30)
	v_mul_f32_e32 v84, 0x42800000, v84
	v_mov_b32_e32 v175, v129
	s_waitcnt vmcnt(27)
	v_mul_f32_e32 v48, 0x42800000, v48
	s_waitcnt vmcnt(26)
	v_mul_f32_e32 v52, 0x42800000, v52
	v_mov_b32_e32 v176, v129
	s_waitcnt vmcnt(23)
	v_mul_f32_e32 v16, 0x42800000, v16
	s_waitcnt vmcnt(22)
	v_mul_f32_e32 v20, 0x42800000, v20
	v_mov_b32_e32 v177, v129
	v_cvt_pk_fp8_f32 v174, v108, v112
	v_cvt_pk_fp8_f32 v175, v80, v84
	v_cvt_pk_fp8_f32 v176, v48, v52
	v_cvt_pk_fp8_f32 v177, v16, v20
	v_mul_f32_e32 v116, 0x42800000, v116
	v_mul_f32_e32 v120, 0x42800000, v120
	v_mul_f32_e32 v88, 0x42800000, v88
	v_mul_f32_e32 v92, 0x42800000, v92
	v_mul_f32_e32 v56, 0x42800000, v56
	v_mul_f32_e32 v60, 0x42800000, v60
	s_waitcnt vmcnt(21)
	v_mul_f32_e32 v24, 0x42800000, v24
	s_waitcnt vmcnt(20)
	v_mul_f32_e32 v28, 0x42800000, v28
	v_cvt_pk_fp8_f32 v174, v116, v120 op_sel:[0,0,1]
	v_cvt_pk_fp8_f32 v175, v88, v92 op_sel:[0,0,1]
	v_cvt_pk_fp8_f32 v176, v56, v60 op_sel:[0,0,1]
	v_cvt_pk_fp8_f32 v177, v24, v28 op_sel:[0,0,1]
	v_mul_f32_e32 v16, 0x42800000, v109
	v_mul_f32_e32 v20, 0x42800000, v113
	v_mul_f32_e32 v24, 0x42800000, v117
	ds_write_b128 v204, v[174:177]
	v_mov_b32_e32 v174, v129
	v_cvt_pk_fp8_f32 v174, v16, v20
	v_mul_f32_e32 v16, 0x42800000, v81
	v_mul_f32_e32 v20, 0x42800000, v85
	v_mov_b32_e32 v175, v129
	v_cvt_pk_fp8_f32 v175, v16, v20
	v_mul_f32_e32 v16, 0x42800000, v49
	v_mul_f32_e32 v20, 0x42800000, v53
	v_mov_b32_e32 v176, v129
	v_cvt_pk_fp8_f32 v176, v16, v20
	v_mul_f32_e32 v16, 0x42800000, v17
	v_mul_f32_e32 v17, 0x42800000, v21
	v_mov_b32_e32 v177, v129
	v_cvt_pk_fp8_f32 v177, v16, v17
	v_mul_f32_e32 v28, 0x42800000, v121
	v_cvt_pk_fp8_f32 v174, v24, v28 op_sel:[0,0,1]
	v_mul_f32_e32 v24, 0x42800000, v89
	v_mul_f32_e32 v28, 0x42800000, v93
	v_cvt_pk_fp8_f32 v175, v24, v28 op_sel:[0,0,1]
	v_mul_f32_e32 v24, 0x42800000, v57
	v_mul_f32_e32 v28, 0x42800000, v61
	v_mul_f32_e32 v20, 0x42800000, v25
	v_mul_f32_e32 v21, 0x42800000, v29
	v_cvt_pk_fp8_f32 v176, v24, v28 op_sel:[0,0,1]
	v_cvt_pk_fp8_f32 v177, v20, v21 op_sel:[0,0,1]
	v_mul_f32_e32 v16, 0x42800000, v110
	v_mul_f32_e32 v17, 0x42800000, v114
	v_mul_f32_e32 v20, 0x42800000, v118
	ds_write_b128 v204, v[174:177] offset:128
	v_mov_b32_e32 v174, v129
	v_cvt_pk_fp8_f32 v174, v16, v17
	v_mul_f32_e32 v16, 0x42800000, v82
	v_mul_f32_e32 v17, 0x42800000, v86
	v_mov_b32_e32 v175, v129
	v_cvt_pk_fp8_f32 v175, v16, v17
	v_mul_f32_e32 v16, 0x42800000, v50
	v_mul_f32_e32 v17, 0x42800000, v54
	v_mov_b32_e32 v176, v129
	v_cvt_pk_fp8_f32 v176, v16, v17
	v_mul_f32_e32 v16, 0x42800000, v18
	v_mul_f32_e32 v17, 0x42800000, v22
	v_mov_b32_e32 v177, v129
	v_mul_f32_e32 v21, 0x42800000, v122
	v_cvt_pk_fp8_f32 v177, v16, v17
	v_cvt_pk_fp8_f32 v174, v20, v21 op_sel:[0,0,1]
	v_mul_f32_e32 v20, 0x42800000, v90
	v_mul_f32_e32 v21, 0x42800000, v94
	v_cvt_pk_fp8_f32 v175, v20, v21 op_sel:[0,0,1]
	v_mul_f32_e32 v20, 0x42800000, v58
	v_mul_f32_e32 v21, 0x42800000, v62
	v_cvt_pk_fp8_f32 v176, v20, v21 op_sel:[0,0,1]
	v_mul_f32_e32 v18, 0x42800000, v26
	v_mul_f32_e32 v20, 0x42800000, v30
	v_cvt_pk_fp8_f32 v177, v18, v20 op_sel:[0,0,1]
	v_mul_f32_e32 v17, 0x42800000, v111
	v_mul_f32_e32 v18, 0x42800000, v115
	v_mov_b32_e32 v16, v129
	v_cvt_pk_fp8_f32 v16, v17, v18
	v_mul_f32_e32 v20, 0x42800000, v119
	v_mul_f32_e32 v21, 0x42800000, v123
	v_mul_f32_e32 v18, 0x42800000, v83
	v_cvt_pk_fp8_f32 v16, v20, v21 op_sel:[0,0,1]
	v_mul_f32_e32 v20, 0x42800000, v87
	v_mov_b32_e32 v17, v129
	v_cvt_pk_fp8_f32 v17, v18, v20
	v_mul_f32_e32 v21, 0x42800000, v91
	v_mul_f32_e32 v22, 0x42800000, v95
	v_mul_f32_e32 v20, 0x42800000, v51
	v_cvt_pk_fp8_f32 v17, v21, v22 op_sel:[0,0,1]
	v_mul_f32_e32 v21, 0x42800000, v55
	v_mov_b32_e32 v18, v129
	v_cvt_pk_fp8_f32 v18, v20, v21
	v_mul_f32_e32 v20, 0x42800000, v19
	v_mul_f32_e32 v21, 0x42800000, v23
	v_mov_b32_e32 v19, v129
	v_cvt_pk_fp8_f32 v19, v20, v21
	v_mul_f32_e32 v22, 0x42800000, v59
	v_mul_f32_e32 v24, 0x42800000, v63
	v_cvt_pk_fp8_f32 v18, v22, v24 op_sel:[0,0,1]
	v_mul_f32_e32 v22, 0x42800000, v27
	v_mul_f32_e32 v23, 0x42800000, v31
	v_cvt_pk_fp8_f32 v19, v22, v23 op_sel:[0,0,1]
	ds_write_b128 v204, v[174:177] offset:256
	ds_write_b128 v204, v[16:19] offset:384
	s_waitcnt lgkmcnt(0)
	s_barrier
; #define LAS __attribute__((address_space(3)))
; __device__ __forceinline__ unsigned pack4_fp8(float a, float b, float c, float d) { int r = 0; r = __builtin_amdgcn_cvt_pk_fp8_f32(a, b, r, false); r = __builtin_amdgcn_cvt_pk_fp8_f32(c, d, r, true); return (unsigned)r; }
; __device__ __forceinline__ void cvt8_to_lds(const f32x4 (&v)[16], LAS unsigned char* tile, int lane, int wv) {
; #pragma unroll
;     for (int i = 0; i < 4; ++i) { u32x4 w; w.x = pack4_fp8(v[0][i] * W8_SCALE, v[1][i] * W8_SCALE, v[2][i] * W8_SCALE, v[3][i] * W8_SCALE); w.y = pack4_fp8(v[4][i] * W8_SCALE, v[5][i] * W8_SCALE, v[6][i] * W8_SCALE, v[7][i] * W8_SCALE);
;         w.z = pack4_fp8(v[8][i] * W8_SCALE, v[9][i] * W8_SCALE, v[10][i] * W8_SCALE, v[11][i] * W8_SCALE); w.w = pack4_fp8(v[12][i] * W8_SCALE, v[13][i] * W8_SCALE, v[14][i] * W8_SCALE, v[15][i] * W8_SCALE);
;         *(LAS u32x4*)(tile + (4 * lane + i) * 128 + ((wv ^ (lane & 7)) << 4)) = w; }
; }
; __device__ __forceinline__ void cvt8_from_lds(const LAS unsigned char* tile, fp8_t* d, int ld_dst, int tid) {
;     const int c = tid & 7;
; #pragma unroll
;     for (int q = 0; q < 4; ++q) { const int r = (tid >> 3) + 64 * q; const u32x4 w = *(const LAS u32x4*)(tile + r * 128 + ((c ^ ((r >> 2) & 7)) << 4));
;         __builtin_nontemporal_store(w, (u32x4*)(d + (size_t)r * ld_dst + 16 * c)); }
; }
; __device__ __forceinline__ void cvt_item_lds(const float* src, int ld_src, fp8_t* dst, int ld_dst, LAS unsigned char* lds, int tid, int wv) {
;     const int lane = tid & 63;
;     const float* s = src + (size_t)(16 * wv) * ld_src + 4 * lane;
;     f32x4 va[16], vb[16];
;     cvt8_load(va, s, ld_src);
; #pragma unroll
;     for (int t = 0; t < 8; t += 2) {
;         cvt8_load(vb, s + (t + 1) * 256, ld_src); __builtin_amdgcn_sched_barrier(0);
;         cvt8_to_lds(va, lds, lane, wv); CVT_LDS_BAR(); __builtin_amdgcn_sched_barrier(0);
;         cvt8_from_lds(lds, dst + (size_t)(t * 256) * ld_dst, ld_dst, tid); __builtin_amdgcn_sched_barrier(0);
;         if (t + 2 < 8) { cvt8_load(va, s + (t + 2) * 256, ld_src); __builtin_amdgcn_sched_barrier(0); }
;         cvt8_to_lds(vb, lds + 32768, lane, wv); CVT_LDS_BAR(); __builtin_amdgcn_sched_barrier(0);
;         cvt8_from_lds(lds + 32768, dst + (size_t)((t + 1) * 256) * ld_dst, ld_dst, tid); __builtin_amdgcn_sched_barrier(0);
	ds_read_b128 v[16:19], v205
	v_lshl_add_u64 v[20:21], v[140:141], 0, s[40:41]
	v_lshl_add_u64 v[22:23], v[20:21], 0, v[132:133]
	s_waitcnt lgkmcnt(0)
	global_store_dwordx4 v[22:23], v[16:19], off nt
	ds_read_b128 v[16:19], v206
	v_lshl_add_u64 v[22:23], v[20:21], 0, v[134:135]
	s_waitcnt lgkmcnt(0)
	global_store_dwordx4 v[22:23], v[16:19], off nt
	ds_read_b128 v[16:19], v207
	v_lshl_add_u64 v[22:23], v[20:21], 0, v[136:137]
	v_lshl_add_u64 v[20:21], v[20:21], 0, v[138:139]
	s_waitcnt lgkmcnt(0)
	global_store_dwordx4 v[22:23], v[16:19], off nt
	ds_read_b128 v[16:19], v208
	s_waitcnt lgkmcnt(0)
	global_store_dwordx4 v[20:21], v[16:19], off nt
	global_load_dwordx4 v[108:111], v[172:173], off offset:2048 nt
	global_load_dwordx4 v[112:115], v[142:143], off offset:2048 nt
	global_load_dwordx4 v[116:119], v[144:145], off offset:2048 nt
	global_load_dwordx4 v[120:123], v[146:147], off offset:2048 nt
	global_load_dwordx4 v[80:83], v[148:149], off offset:2048 nt
	global_load_dwordx4 v[84:87], v[150:151], off offset:2048 nt
	global_load_dwordx4 v[88:91], v[152:153], off offset:2048 nt
	global_load_dwordx4 v[92:95], v[154:155], off offset:2048 nt
	global_load_dwordx4 v[48:51], v[156:157], off offset:2048 nt
	global_load_dwordx4 v[52:55], v[158:159], off offset:2048 nt
	global_load_dwordx4 v[56:59], v[160:161], off offset:2048 nt
	global_load_dwordx4 v[60:63], v[162:163], off offset:2048 nt
	global_load_dwordx4 v[16:19], v[164:165], off offset:2048 nt
	global_load_dwordx4 v[20:23], v[166:167], off offset:2048 nt
	global_load_dwordx4 v[24:27], v[168:169], off offset:2048 nt
	global_load_dwordx4 v[28:31], v[170:171], off offset:2048 nt
	s_waitcnt vmcnt(35)
	v_mul_f32_e32 v96, 0x42800000, v96
	s_waitcnt vmcnt(34)
	v_mul_f32_e32 v100, 0x42800000, v100
	v_mov_b32_e32 v174, v129
	s_waitcnt vmcnt(31)
	v_mul_f32_e32 v64, 0x42800000, v64
	s_waitcnt vmcnt(30)
	v_mul_f32_e32 v68, 0x42800000, v68
	v_mov_b32_e32 v175, v129
	s_waitcnt vmcnt(27)
	v_mul_f32_e32 v32, 0x42800000, v32
	s_waitcnt vmcnt(26)
	v_mul_f32_e32 v36, 0x42800000, v36
	v_mov_b32_e32 v176, v129
	s_waitcnt vmcnt(23)
	v_mul_f32_e32 v0, 0x42800000, v0
	s_waitcnt vmcnt(22)
	v_mul_f32_e32 v4, 0x42800000, v4
	v_mov_b32_e32 v177, v129
	v_cvt_pk_fp8_f32 v174, v96, v100
	v_cvt_pk_fp8_f32 v175, v64, v68
	v_cvt_pk_fp8_f32 v176, v32, v36
	v_cvt_pk_fp8_f32 v177, v0, v4
	v_mul_f32_e32 v104, 0x42800000, v104
	v_mul_f32_e32 v124, 0x42800000, v124
	v_mul_f32_e32 v72, 0x42800000, v72
	v_mul_f32_e32 v76, 0x42800000, v76
	v_mul_f32_e32 v40, 0x42800000, v40
	v_mul_f32_e32 v44, 0x42800000, v44
	s_waitcnt vmcnt(21)
	v_mul_f32_e32 v8, 0x42800000, v8
	s_waitcnt vmcnt(20)
	v_mul_f32_e32 v12, 0x42800000, v12
	v_cvt_pk_fp8_f32 v174, v104, v124 op_sel:[0,0,1]
	v_cvt_pk_fp8_f32 v175, v72, v76 op_sel:[0,0,1]
	v_cvt_pk_fp8_f32 v176, v40, v44 op_sel:[0,0,1]
	v_cvt_pk_fp8_f32 v177, v8, v12 op_sel:[0,0,1]
	v_mul_f32_e32 v0, 0x42800000, v97
	v_mul_f32_e32 v4, 0x42800000, v101
	v_mul_f32_e32 v8, 0x42800000, v105
	ds_write_b128 v204, v[174:177] offset:32768
	v_mov_b32_e32 v174, v129
	v_cvt_pk_fp8_f32 v174, v0, v4
	v_mul_f32_e32 v0, 0x42800000, v65
	v_mul_f32_e32 v4, 0x42800000, v69
	v_mov_b32_e32 v175, v129
	v_cvt_pk_fp8_f32 v175, v0, v4
	v_mul_f32_e32 v0, 0x42800000, v33
	v_mul_f32_e32 v4, 0x42800000, v37
	v_mov_b32_e32 v176, v129
	v_cvt_pk_fp8_f32 v176, v0, v4
	v_mul_f32_e32 v0, 0x42800000, v1
	v_mul_f32_e32 v1, 0x42800000, v5
	v_mov_b32_e32 v177, v129
	v_cvt_pk_fp8_f32 v177, v0, v1
	v_mul_f32_e32 v12, 0x42800000, v125
	v_cvt_pk_fp8_f32 v174, v8, v12 op_sel:[0,0,1]
	v_mul_f32_e32 v8, 0x42800000, v73
	v_mul_f32_e32 v12, 0x42800000, v77
	v_cvt_pk_fp8_f32 v175, v8, v12 op_sel:[0,0,1]
	v_mul_f32_e32 v8, 0x42800000, v41
	v_mul_f32_e32 v12, 0x42800000, v45
	v_mul_f32_e32 v4, 0x42800000, v9
	v_mul_f32_e32 v5, 0x42800000, v13
	v_cvt_pk_fp8_f32 v176, v8, v12 op_sel:[0,0,1]
	v_cvt_pk_fp8_f32 v177, v4, v5 op_sel:[0,0,1]
	v_mul_f32_e32 v0, 0x42800000, v98
	v_mul_f32_e32 v1, 0x42800000, v102
	v_mul_f32_e32 v4, 0x42800000, v106
	ds_write_b128 v204, v[174:177] offset:32896
	v_mov_b32_e32 v174, v129
	v_cvt_pk_fp8_f32 v174, v0, v1
	v_mul_f32_e32 v0, 0x42800000, v66
	v_mul_f32_e32 v1, 0x42800000, v70
	v_mov_b32_e32 v175, v129
	v_cvt_pk_fp8_f32 v175, v0, v1
	v_mul_f32_e32 v0, 0x42800000, v34
	v_mul_f32_e32 v1, 0x42800000, v38
	v_mov_b32_e32 v176, v129
	v_cvt_pk_fp8_f32 v176, v0, v1
	v_mul_f32_e32 v0, 0x42800000, v2
	v_mul_f32_e32 v1, 0x42800000, v6
	v_mov_b32_e32 v177, v129
	v_mul_f32_e32 v5, 0x42800000, v126
	v_cvt_pk_fp8_f32 v177, v0, v1
	v_cvt_pk_fp8_f32 v174, v4, v5 op_sel:[0,0,1]
	v_mul_f32_e32 v4, 0x42800000, v74
	v_mul_f32_e32 v5, 0x42800000, v78
	v_cvt_pk_fp8_f32 v175, v4, v5 op_sel:[0,0,1]
	v_mul_f32_e32 v4, 0x42800000, v42
	v_mul_f32_e32 v5, 0x42800000, v46
	v_cvt_pk_fp8_f32 v176, v4, v5 op_sel:[0,0,1]
	v_mul_f32_e32 v2, 0x42800000, v10
	v_mul_f32_e32 v4, 0x42800000, v14
	v_cvt_pk_fp8_f32 v177, v2, v4 op_sel:[0,0,1]
	v_mul_f32_e32 v1, 0x42800000, v99
	v_mul_f32_e32 v2, 0x42800000, v103
	v_mov_b32_e32 v0, v129
	v_cvt_pk_fp8_f32 v0, v1, v2
	v_mul_f32_e32 v4, 0x42800000, v107
	v_mul_f32_e32 v5, 0x42800000, v127
	v_mul_f32_e32 v2, 0x42800000, v67
	v_cvt_pk_fp8_f32 v0, v4, v5 op_sel:[0,0,1]
	v_mul_f32_e32 v4, 0x42800000, v71
	v_mov_b32_e32 v1, v129
	v_cvt_pk_fp8_f32 v1, v2, v4
	v_mul_f32_e32 v5, 0x42800000, v75
	v_mul_f32_e32 v6, 0x42800000, v79
	v_mul_f32_e32 v4, 0x42800000, v35
	v_cvt_pk_fp8_f32 v1, v5, v6 op_sel:[0,0,1]
	v_mul_f32_e32 v5, 0x42800000, v39
	v_mov_b32_e32 v2, v129
	v_cvt_pk_fp8_f32 v2, v4, v5
	v_mul_f32_e32 v4, 0x42800000, v3
	v_mul_f32_e32 v5, 0x42800000, v7
	v_mov_b32_e32 v3, v129
	v_cvt_pk_fp8_f32 v3, v4, v5
	v_mul_f32_e32 v6, 0x42800000, v43
	v_mul_f32_e32 v8, 0x42800000, v47
	v_cvt_pk_fp8_f32 v2, v6, v8 op_sel:[0,0,1]
	v_mul_f32_e32 v6, 0x42800000, v11
	v_mul_f32_e32 v7, 0x42800000, v15
	v_cvt_pk_fp8_f32 v3, v6, v7 op_sel:[0,0,1]
	ds_write_b128 v204, v[174:177] offset:33024
	ds_write_b128 v204, v[0:3] offset:33152
	s_waitcnt lgkmcnt(0)
	s_barrier
; #define LAS __attribute__((address_space(3)))
; __device__ __forceinline__ unsigned pack4_fp8(float a, float b, float c, float d) { int r = 0; r = __builtin_amdgcn_cvt_pk_fp8_f32(a, b, r, false); r = __builtin_amdgcn_cvt_pk_fp8_f32(c, d, r, true); return (unsigned)r; }
; __device__ __forceinline__ void cvt8_to_lds(const f32x4 (&v)[16], LAS unsigned char* tile, int lane, int wv) {
; #pragma unroll
;     for (int i = 0; i < 4; ++i) { u32x4 w; w.x = pack4_fp8(v[0][i] * W8_SCALE, v[1][i] * W8_SCALE, v[2][i] * W8_SCALE, v[3][i] * W8_SCALE); w.y = pack4_fp8(v[4][i] * W8_SCALE, v[5][i] * W8_SCALE, v[6][i] * W8_SCALE, v[7][i] * W8_SCALE);
;         w.z = pack4_fp8(v[8][i] * W8_SCALE, v[9][i] * W8_SCALE, v[10][i] * W8_SCALE, v[11][i] * W8_SCALE); w.w = pack4_fp8(v[12][i] * W8_SCALE, v[13][i] * W8_SCALE, v[14][i] * W8_SCALE, v[15][i] * W8_SCALE);
;         *(LAS u32x4*)(tile + (4 * lane + i) * 128 + ((wv ^ (lane & 7)) << 4)) = w; }
; }
; __device__ __forceinline__ void cvt8_from_lds(const LAS unsigned char* tile, fp8_t* d, int ld_dst, int tid) {
;     const int c = tid & 7;
; #pragma unroll
;     for (int q = 0; q < 4; ++q) { const int r = (tid >> 3) + 64 * q; const u32x4 w = *(const LAS u32x4*)(tile + r * 128 + ((c ^ ((r >> 2) & 7)) << 4));
;         __builtin_nontemporal_store(w, (u32x4*)(d + (size_t)r * ld_dst + 16 * c)); }
; }
; __device__ __forceinline__ void cvt_item_lds(const float* src, int ld_src, fp8_t* dst, int ld_dst, LAS unsigned char* lds, int tid, int wv) {
;     const int lane = tid & 63;
;     const float* s = src + (size_t)(16 * wv) * ld_src + 4 * lane;
;     f32x4 va[16], vb[16];
;     cvt8_load(va, s, ld_src);
; #pragma unroll
;     for (int t = 0; t < 8; t += 2) {
;         cvt8_load(vb, s + (t + 1) * 256, ld_src); __builtin_amdgcn_sched_barrier(0);
;         cvt8_to_lds(va, lds, lane, wv); CVT_LDS_BAR(); __builtin_amdgcn_sched_barrier(0);
;         cvt8_from_lds(lds, dst + (size_t)(t * 256) * ld_dst, ld_dst, tid); __builtin_amdgcn_sched_barrier(0);
;         if (t + 2 < 8) { cvt8_load(va, s + (t + 2) * 256, ld_src); __builtin_amdgcn_sched_barrier(0); }
;         cvt8_to_lds(vb, lds + 32768, lane, wv); CVT_LDS_BAR(); __builtin_amdgcn_sched_barrier(0);
;         cvt8_from_lds(lds + 32768, dst + (size_t)((t + 1) * 256) * ld_dst, ld_dst, tid); __builtin_amdgcn_sched_barrier(0);
	ds_read_b128 v[0:3], v205 offset:32768
	v_lshl_add_u64 v[4:5], v[140:141], 0, s[42:43]
	v_lshl_add_u64 v[6:7], v[4:5], 0, v[132:133]
	s_waitcnt lgkmcnt(0)
	global_store_dwordx4 v[6:7], v[0:3], off nt
	ds_read_b128 v[0:3], v206 offset:32768
	v_lshl_add_u64 v[6:7], v[4:5], 0, v[134:135]
	s_waitcnt lgkmcnt(0)
	global_store_dwordx4 v[6:7], v[0:3], off nt
	ds_read_b128 v[0:3], v207 offset:32768
	v_lshl_add_u64 v[6:7], v[4:5], 0, v[136:137]
	v_lshl_add_u64 v[4:5], v[4:5], 0, v[138:139]
	s_waitcnt lgkmcnt(0)
	global_store_dwordx4 v[6:7], v[0:3], off nt
	ds_read_b128 v[0:3], v208 offset:32768
	s_waitcnt lgkmcnt(0)
	global_store_dwordx4 v[4:5], v[0:3], off nt
	global_load_dwordx4 v[96:99], v[172:173], off offset:3072 nt
	global_load_dwordx4 v[100:103], v[142:143], off offset:3072 nt
	global_load_dwordx4 v[104:107], v[144:145], off offset:3072 nt
	global_load_dwordx4 v[124:127], v[146:147], off offset:3072 nt
	global_load_dwordx4 v[64:67], v[148:149], off offset:3072 nt
	global_load_dwordx4 v[68:71], v[150:151], off offset:3072 nt
	global_load_dwordx4 v[72:75], v[152:153], off offset:3072 nt
	global_load_dwordx4 v[76:79], v[154:155], off offset:3072 nt
	global_load_dwordx4 v[32:35], v[156:157], off offset:3072 nt
	global_load_dwordx4 v[36:39], v[158:159], off offset:3072 nt
	global_load_dwordx4 v[40:43], v[160:161], off offset:3072 nt
	global_load_dwordx4 v[44:47], v[162:163], off offset:3072 nt
	global_load_dwordx4 v[0:3], v[164:165], off offset:3072 nt
	global_load_dwordx4 v[4:7], v[166:167], off offset:3072 nt
	global_load_dwordx4 v[8:11], v[168:169], off offset:3072 nt
	global_load_dwordx4 v[12:15], v[170:171], off offset:3072 nt
	s_waitcnt vmcnt(35)
	v_mul_f32_e32 v108, 0x42800000, v108
	s_waitcnt vmcnt(34)
	v_mul_f32_e32 v112, 0x42800000, v112
	v_mov_b32_e32 v142, v129
	s_waitcnt vmcnt(31)
	v_mul_f32_e32 v80, 0x42800000, v80
	s_waitcnt vmcnt(30)
	v_mul_f32_e32 v84, 0x42800000, v84
	v_mov_b32_e32 v143, v129
	s_waitcnt vmcnt(27)
	v_mul_f32_e32 v48, 0x42800000, v48
	s_waitcnt vmcnt(26)
	v_mul_f32_e32 v52, 0x42800000, v52
	v_mov_b32_e32 v144, v129
	s_waitcnt vmcnt(23)
	v_mul_f32_e32 v16, 0x42800000, v16
	s_waitcnt vmcnt(22)
	v_mul_f32_e32 v20, 0x42800000, v20
	v_mov_b32_e32 v145, v129
	v_cvt_pk_fp8_f32 v142, v108, v112
	v_cvt_pk_fp8_f32 v143, v80, v84
	v_cvt_pk_fp8_f32 v144, v48, v52
	v_cvt_pk_fp8_f32 v145, v16, v20
	v_mul_f32_e32 v116, 0x42800000, v116
	v_mul_f32_e32 v120, 0x42800000, v120
	v_mul_f32_e32 v88, 0x42800000, v88
	v_mul_f32_e32 v92, 0x42800000, v92
	v_mul_f32_e32 v56, 0x42800000, v56
	v_mul_f32_e32 v60, 0x42800000, v60
	s_waitcnt vmcnt(21)
	v_mul_f32_e32 v24, 0x42800000, v24
	s_waitcnt vmcnt(20)
	v_mul_f32_e32 v28, 0x42800000, v28
	v_cvt_pk_fp8_f32 v142, v116, v120 op_sel:[0,0,1]
	v_cvt_pk_fp8_f32 v143, v88, v92 op_sel:[0,0,1]
	v_cvt_pk_fp8_f32 v144, v56, v60 op_sel:[0,0,1]
	v_cvt_pk_fp8_f32 v145, v24, v28 op_sel:[0,0,1]
	v_mul_f32_e32 v16, 0x42800000, v109
	v_mul_f32_e32 v20, 0x42800000, v113
	v_mul_f32_e32 v24, 0x42800000, v117
	ds_write_b128 v204, v[142:145]
	v_mov_b32_e32 v142, v129
	v_cvt_pk_fp8_f32 v142, v16, v20
	v_mul_f32_e32 v16, 0x42800000, v81
	v_mul_f32_e32 v20, 0x42800000, v85
	v_mov_b32_e32 v143, v129
	v_cvt_pk_fp8_f32 v143, v16, v20
	v_mul_f32_e32 v16, 0x42800000, v49
	v_mul_f32_e32 v20, 0x42800000, v53
	v_mov_b32_e32 v144, v129
	v_cvt_pk_fp8_f32 v144, v16, v20
	v_mul_f32_e32 v16, 0x42800000, v17
	v_mul_f32_e32 v17, 0x42800000, v21
	v_mov_b32_e32 v145, v129
	v_cvt_pk_fp8_f32 v145, v16, v17
	v_mul_f32_e32 v28, 0x42800000, v121
	v_cvt_pk_fp8_f32 v142, v24, v28 op_sel:[0,0,1]
	v_mul_f32_e32 v24, 0x42800000, v89
	v_mul_f32_e32 v28, 0x42800000, v93
	v_cvt_pk_fp8_f32 v143, v24, v28 op_sel:[0,0,1]
	v_mul_f32_e32 v24, 0x42800000, v57
	v_mul_f32_e32 v28, 0x42800000, v61
	v_mul_f32_e32 v20, 0x42800000, v25
	v_mul_f32_e32 v21, 0x42800000, v29
	v_cvt_pk_fp8_f32 v144, v24, v28 op_sel:[0,0,1]
	v_cvt_pk_fp8_f32 v145, v20, v21 op_sel:[0,0,1]
	v_mul_f32_e32 v16, 0x42800000, v110
	v_mul_f32_e32 v17, 0x42800000, v114
	v_mul_f32_e32 v20, 0x42800000, v118
	ds_write_b128 v204, v[142:145] offset:128
	v_mov_b32_e32 v142, v129
	v_cvt_pk_fp8_f32 v142, v16, v17
	v_mul_f32_e32 v16, 0x42800000, v82
	v_mul_f32_e32 v17, 0x42800000, v86
	v_mov_b32_e32 v143, v129
	v_cvt_pk_fp8_f32 v143, v16, v17
	v_mul_f32_e32 v16, 0x42800000, v50
	v_mul_f32_e32 v17, 0x42800000, v54
	v_mov_b32_e32 v144, v129
	v_cvt_pk_fp8_f32 v144, v16, v17
	v_mul_f32_e32 v16, 0x42800000, v18
	v_mul_f32_e32 v17, 0x42800000, v22
	v_mov_b32_e32 v145, v129
	v_mul_f32_e32 v21, 0x42800000, v122
	v_cvt_pk_fp8_f32 v145, v16, v17
	v_cvt_pk_fp8_f32 v142, v20, v21 op_sel:[0,0,1]
	v_mul_f32_e32 v20, 0x42800000, v90
	v_mul_f32_e32 v21, 0x42800000, v94
	v_cvt_pk_fp8_f32 v143, v20, v21 op_sel:[0,0,1]
	v_mul_f32_e32 v20, 0x42800000, v58
	v_mul_f32_e32 v21, 0x42800000, v62
	v_cvt_pk_fp8_f32 v144, v20, v21 op_sel:[0,0,1]
	v_mul_f32_e32 v18, 0x42800000, v26
	v_mul_f32_e32 v20, 0x42800000, v30
	v_cvt_pk_fp8_f32 v145, v18, v20 op_sel:[0,0,1]
	v_mul_f32_e32 v17, 0x42800000, v111
	v_mul_f32_e32 v18, 0x42800000, v115
	v_mov_b32_e32 v16, v129
	v_cvt_pk_fp8_f32 v16, v17, v18
	v_mul_f32_e32 v20, 0x42800000, v119
	v_mul_f32_e32 v21, 0x42800000, v123
	v_mul_f32_e32 v18, 0x42800000, v83
	v_cvt_pk_fp8_f32 v16, v20, v21 op_sel:[0,0,1]
	v_mul_f32_e32 v20, 0x42800000, v87
	v_mov_b32_e32 v17, v129
	v_cvt_pk_fp8_f32 v17, v18, v20
	v_mul_f32_e32 v21, 0x42800000, v91
	v_mul_f32_e32 v22, 0x42800000, v95
	v_mul_f32_e32 v20, 0x42800000, v51
	v_cvt_pk_fp8_f32 v17, v21, v22 op_sel:[0,0,1]
	v_mul_f32_e32 v21, 0x42800000, v55
	v_mov_b32_e32 v18, v129
	v_cvt_pk_fp8_f32 v18, v20, v21
	v_mul_f32_e32 v20, 0x42800000, v19
	v_mul_f32_e32 v21, 0x42800000, v23
	v_mov_b32_e32 v19, v129
	v_cvt_pk_fp8_f32 v19, v20, v21
	v_mul_f32_e32 v22, 0x42800000, v59
	v_mul_f32_e32 v24, 0x42800000, v63
	v_cvt_pk_fp8_f32 v18, v22, v24 op_sel:[0,0,1]
	v_mul_f32_e32 v22, 0x42800000, v27
	v_mul_f32_e32 v23, 0x42800000, v31
	v_cvt_pk_fp8_f32 v19, v22, v23 op_sel:[0,0,1]
	ds_write_b128 v204, v[142:145] offset:256
	ds_write_b128 v204, v[16:19] offset:384
	s_waitcnt lgkmcnt(0)
	s_barrier
; #define LAS __attribute__((address_space(3)))
; __device__ __forceinline__ unsigned pack4_fp8(float a, float b, float c, float d) { int r = 0; r = __builtin_amdgcn_cvt_pk_fp8_f32(a, b, r, false); r = __builtin_amdgcn_cvt_pk_fp8_f32(c, d, r, true); return (unsigned)r; }
; __device__ __forceinline__ void cvt8_to_lds(const f32x4 (&v)[16], LAS unsigned char* tile, int lane, int wv) {
; #pragma unroll
;     for (int i = 0; i < 4; ++i) { u32x4 w; w.x = pack4_fp8(v[0][i] * W8_SCALE, v[1][i] * W8_SCALE, v[2][i] * W8_SCALE, v[3][i] * W8_SCALE); w.y = pack4_fp8(v[4][i] * W8_SCALE, v[5][i] * W8_SCALE, v[6][i] * W8_SCALE, v[7][i] * W8_SCALE);
;         w.z = pack4_fp8(v[8][i] * W8_SCALE, v[9][i] * W8_SCALE, v[10][i] * W8_SCALE, v[11][i] * W8_SCALE); w.w = pack4_fp8(v[12][i] * W8_SCALE, v[13][i] * W8_SCALE, v[14][i] * W8_SCALE, v[15][i] * W8_SCALE);
;         *(LAS u32x4*)(tile + (4 * lane + i) * 128 + ((wv ^ (lane & 7)) << 4)) = w; }
; }
; __device__ __forceinline__ void cvt8_from_lds(const LAS unsigned char* tile, fp8_t* d, int ld_dst, int tid) {
;     const int c = tid & 7;
; #pragma unroll
;     for (int q = 0; q < 4; ++q) { const int r = (tid >> 3) + 64 * q; const u32x4 w = *(const LAS u32x4*)(tile + r * 128 + ((c ^ ((r >> 2) & 7)) << 4));
;         __builtin_nontemporal_store(w, (u32x4*)(d + (size_t)r * ld_dst + 16 * c)); }
; }
; __device__ __forceinline__ void cvt_item_lds(const float* src, int ld_src, fp8_t* dst, int ld_dst, LAS unsigned char* lds, int tid, int wv) {
;     const int lane = tid & 63;
;     const float* s = src + (size_t)(16 * wv) * ld_src + 4 * lane;
;     f32x4 va[16], vb[16];
;     cvt8_load(va, s, ld_src);
; #pragma unroll
;     for (int t = 0; t < 8; t += 2) {
;         cvt8_load(vb, s + (t + 1) * 256, ld_src); __builtin_amdgcn_sched_barrier(0);
;         cvt8_to_lds(va, lds, lane, wv); CVT_LDS_BAR(); __builtin_amdgcn_sched_barrier(0);
;         cvt8_from_lds(lds, dst + (size_t)(t * 256) * ld_dst, ld_dst, tid); __builtin_amdgcn_sched_barrier(0);
;         if (t + 2 < 8) { cvt8_load(va, s + (t + 2) * 256, ld_src); __builtin_amdgcn_sched_barrier(0); }
;         cvt8_to_lds(vb, lds + 32768, lane, wv); CVT_LDS_BAR(); __builtin_amdgcn_sched_barrier(0);
;         cvt8_from_lds(lds + 32768, dst + (size_t)((t + 1) * 256) * ld_dst, ld_dst, tid); __builtin_amdgcn_sched_barrier(0);
	ds_read_b128 v[16:19], v205
	v_lshl_add_u64 v[20:21], v[140:141], 0, s[44:45]
	v_lshl_add_u64 v[22:23], v[20:21], 0, v[132:133]
	s_waitcnt lgkmcnt(0)
	global_store_dwordx4 v[22:23], v[16:19], off nt
	ds_read_b128 v[16:19], v206
	v_lshl_add_u64 v[22:23], v[20:21], 0, v[134:135]
	s_waitcnt lgkmcnt(0)
	global_store_dwordx4 v[22:23], v[16:19], off nt
	ds_read_b128 v[16:19], v207
	v_lshl_add_u64 v[22:23], v[20:21], 0, v[136:137]
	v_lshl_add_u64 v[20:21], v[20:21], 0, v[138:139]
	s_waitcnt lgkmcnt(0)
	global_store_dwordx4 v[22:23], v[16:19], off nt
	ds_read_b128 v[16:19], v208
	s_waitcnt lgkmcnt(0)
	global_store_dwordx4 v[20:21], v[16:19], off nt
	s_waitcnt vmcnt(19)
	s_nop 0
	v_mul_f32_e32 v17, 0x42800000, v96
	s_waitcnt vmcnt(18)
	v_mul_f32_e32 v18, 0x42800000, v100
	v_mov_b32_e32 v16, v129
	v_cvt_pk_fp8_f32 v16, v17, v18
	s_waitcnt vmcnt(17)
	v_mul_f32_e32 v19, 0x42800000, v104
	s_waitcnt vmcnt(16)
	v_mul_f32_e32 v20, 0x42800000, v124
	s_waitcnt vmcnt(15)
	v_mul_f32_e32 v18, 0x42800000, v64
	v_cvt_pk_fp8_f32 v16, v19, v20 op_sel:[0,0,1]
	s_waitcnt vmcnt(14)
	v_mul_f32_e32 v19, 0x42800000, v68
	v_mov_b32_e32 v17, v129
	v_cvt_pk_fp8_f32 v17, v18, v19
	s_waitcnt vmcnt(13)
	v_mul_f32_e32 v20, 0x42800000, v72
	s_waitcnt vmcnt(12)
	v_mul_f32_e32 v21, 0x42800000, v76
	s_waitcnt vmcnt(11)
	v_mul_f32_e32 v19, 0x42800000, v32
	v_cvt_pk_fp8_f32 v17, v20, v21 op_sel:[0,0,1]
	s_waitcnt vmcnt(10)
	v_mul_f32_e32 v20, 0x42800000, v36
	v_mov_b32_e32 v18, v129
	v_cvt_pk_fp8_f32 v18, v19, v20
	s_waitcnt vmcnt(7)
	v_mul_f32_e32 v0, 0x42800000, v0
	s_waitcnt vmcnt(6)
	v_mul_f32_e32 v4, 0x42800000, v4
	v_mov_b32_e32 v19, v129
	v_cvt_pk_fp8_f32 v19, v0, v4
	v_mul_f32_e32 v21, 0x42800000, v40
	v_mul_f32_e32 v22, 0x42800000, v44
	s_waitcnt vmcnt(5)
	v_mul_f32_e32 v8, 0x42800000, v8
	s_waitcnt vmcnt(4)
	v_mul_f32_e32 v12, 0x42800000, v12
	v_cvt_pk_fp8_f32 v18, v21, v22 op_sel:[0,0,1]
	v_cvt_pk_fp8_f32 v19, v8, v12 op_sel:[0,0,1]
	v_mul_f32_e32 v0, 0x42800000, v97
	v_mul_f32_e32 v4, 0x42800000, v101
	v_mul_f32_e32 v8, 0x42800000, v105
	ds_write_b128 v204, v[16:19] offset:32768
	v_mov_b32_e32 v16, v129
	v_cvt_pk_fp8_f32 v16, v0, v4
	v_mul_f32_e32 v0, 0x42800000, v65
	v_mul_f32_e32 v4, 0x42800000, v69
	v_mov_b32_e32 v17, v129
	v_cvt_pk_fp8_f32 v17, v0, v4
	v_mul_f32_e32 v0, 0x42800000, v33
	v_mul_f32_e32 v4, 0x42800000, v37
	v_mov_b32_e32 v18, v129
	v_cvt_pk_fp8_f32 v18, v0, v4
	v_mul_f32_e32 v0, 0x42800000, v1
	v_mul_f32_e32 v1, 0x42800000, v5
	v_mov_b32_e32 v19, v129
	v_cvt_pk_fp8_f32 v19, v0, v1
	v_mul_f32_e32 v12, 0x42800000, v125
	v_cvt_pk_fp8_f32 v16, v8, v12 op_sel:[0,0,1]
	v_mul_f32_e32 v8, 0x42800000, v73
	v_mul_f32_e32 v12, 0x42800000, v77
	v_cvt_pk_fp8_f32 v17, v8, v12 op_sel:[0,0,1]
	v_mul_f32_e32 v8, 0x42800000, v41
	v_mul_f32_e32 v12, 0x42800000, v45
	v_mul_f32_e32 v4, 0x42800000, v9
	v_mul_f32_e32 v5, 0x42800000, v13
	v_cvt_pk_fp8_f32 v18, v8, v12 op_sel:[0,0,1]
	v_cvt_pk_fp8_f32 v19, v4, v5 op_sel:[0,0,1]
	v_mul_f32_e32 v0, 0x42800000, v98
	v_mul_f32_e32 v1, 0x42800000, v102
	v_mul_f32_e32 v4, 0x42800000, v106
	ds_write_b128 v204, v[16:19] offset:32896
	v_mov_b32_e32 v16, v129
	v_cvt_pk_fp8_f32 v16, v0, v1
	v_mul_f32_e32 v0, 0x42800000, v66
	v_mul_f32_e32 v1, 0x42800000, v70
	v_mov_b32_e32 v17, v129
	v_cvt_pk_fp8_f32 v17, v0, v1
	v_mul_f32_e32 v0, 0x42800000, v34
	v_mul_f32_e32 v1, 0x42800000, v38
	v_mov_b32_e32 v18, v129
	v_cvt_pk_fp8_f32 v18, v0, v1
	v_mul_f32_e32 v0, 0x42800000, v2
	v_mul_f32_e32 v1, 0x42800000, v6
	v_mov_b32_e32 v19, v129
	v_mul_f32_e32 v5, 0x42800000, v126
	v_cvt_pk_fp8_f32 v19, v0, v1
	v_cvt_pk_fp8_f32 v16, v4, v5 op_sel:[0,0,1]
	v_mul_f32_e32 v4, 0x42800000, v74
	v_mul_f32_e32 v5, 0x42800000, v78
	v_cvt_pk_fp8_f32 v17, v4, v5 op_sel:[0,0,1]
	v_mul_f32_e32 v4, 0x42800000, v42
	v_mul_f32_e32 v5, 0x42800000, v46
	v_cvt_pk_fp8_f32 v18, v4, v5 op_sel:[0,0,1]
	v_mul_f32_e32 v2, 0x42800000, v10
	v_mul_f32_e32 v4, 0x42800000, v14
	v_cvt_pk_fp8_f32 v19, v2, v4 op_sel:[0,0,1]
	v_mul_f32_e32 v1, 0x42800000, v99
	v_mul_f32_e32 v2, 0x42800000, v103
	v_mov_b32_e32 v0, v129
	v_cvt_pk_fp8_f32 v0, v1, v2
	v_mul_f32_e32 v4, 0x42800000, v107
	v_mul_f32_e32 v5, 0x42800000, v127
	v_mul_f32_e32 v2, 0x42800000, v67
	v_cvt_pk_fp8_f32 v0, v4, v5 op_sel:[0,0,1]
	v_mul_f32_e32 v4, 0x42800000, v71
	v_mov_b32_e32 v1, v129
	v_cvt_pk_fp8_f32 v1, v2, v4
	v_mul_f32_e32 v5, 0x42800000, v75
	v_mul_f32_e32 v6, 0x42800000, v79
	v_mul_f32_e32 v4, 0x42800000, v35
	v_cvt_pk_fp8_f32 v1, v5, v6 op_sel:[0,0,1]
	v_mul_f32_e32 v5, 0x42800000, v39
	v_mov_b32_e32 v2, v129
	v_cvt_pk_fp8_f32 v2, v4, v5
	v_mul_f32_e32 v4, 0x42800000, v3
	v_mul_f32_e32 v5, 0x42800000, v7
	v_mov_b32_e32 v3, v129
	v_cvt_pk_fp8_f32 v3, v4, v5
	v_mul_f32_e32 v6, 0x42800000, v43
	v_mul_f32_e32 v8, 0x42800000, v47
	v_cvt_pk_fp8_f32 v2, v6, v8 op_sel:[0,0,1]
	v_mul_f32_e32 v6, 0x42800000, v11
	v_mul_f32_e32 v7, 0x42800000, v15
	v_cvt_pk_fp8_f32 v3, v6, v7 op_sel:[0,0,1]
	ds_write_b128 v204, v[16:19] offset:33024
	ds_write_b128 v204, v[0:3] offset:33152
	s_waitcnt lgkmcnt(0)
	s_barrier
	ds_read_b128 v[0:3], v205 offset:32768
	v_lshl_add_u64 v[4:5], v[140:141], 0, s[46:47]
	v_lshl_add_u64 v[6:7], v[4:5], 0, v[132:133]
	s_waitcnt lgkmcnt(0)
	global_store_dwordx4 v[6:7], v[0:3], off nt
	ds_read_b128 v[0:3], v206 offset:32768
	v_lshl_add_u64 v[6:7], v[4:5], 0, v[134:135]
	s_waitcnt lgkmcnt(0)
	global_store_dwordx4 v[6:7], v[0:3], off nt
	ds_read_b128 v[0:3], v207 offset:32768
	v_lshl_add_u64 v[6:7], v[4:5], 0, v[136:137]
	v_lshl_add_u64 v[4:5], v[4:5], 0, v[138:139]
	s_waitcnt lgkmcnt(0)
	global_store_dwordx4 v[6:7], v[0:3], off nt
	ds_read_b128 v[0:3], v208 offset:32768
	s_waitcnt lgkmcnt(0)
	global_store_dwordx4 v[4:5], v[0:3], off nt
	s_mov_b64 s[48:49], 0

; __device__ __forceinline__ void conv_queue(const Params& p, LAS unsigned char* lds, const int wave, const int cw, const int first, const int last, const int slot_off = LDS_MISC) {
;     ...
;         __syncthreads();
;         if (tid == 0) *slot = first + (int)atomicAdd(&p.ctl[cw], 1u);
;         __syncthreads();
;         const int it = *slot;
;         if (it >= last) break;
.LBB0_1251:
	s_or_b64 exec, exec, s[52:53]
	s_waitcnt vmcnt(0)
	v_readfirstlane_b32 s2, v1
	v_mov_b32_e32 v1, s13
	s_nop 0
	v_add_u32_e32 v0, s2, v0
	v_add_u32_e32 v0, 0x4a0, v0
	ds_write_b32 v1, v0

; __device__ __forceinline__ void conv_queue(const Params& p, LAS unsigned char* lds, const int wave, const int cw, const int first, const int last, const int slot_off = LDS_MISC) {
;     ...
;         __syncthreads();
;         if (tid == 0) *slot = first + (int)atomicAdd(&p.ctl[cw], 1u);
;         __syncthreads();
;         const int it = *slot;
;         if (it >= last) break;
.LBB0_1276:
	s_or_b64 exec, exec, s[50:51]
	s_waitcnt vmcnt(0)
	v_readfirstlane_b32 s2, v1
	v_mov_b32_e32 v1, s13
	s_nop 0
	v_add_u32_e32 v0, s2, v0
	v_add_u32_e32 v0, 0x4a0, v0
	ds_write_b32 v1, v0
